# K-loop fragment ds_reads of the A-side stage use immediate offsets (per-lane base +0x10000 once per phase) instead of a v_add_u32 per read: 16 VALU fewer per loop body in the load segments, all four G
# speedup vs baseline: 1.0059x; 1.0059x over previous
.LBB0_95:
	s_ashr_i32 s81, s94, 31
	s_ashr_i32 s82, s69, 31
	s_add_u32 s16, s24, 0x1000
	s_addc_u32 s17, s25, 0
	v_writelane_b32 v254, s16, 30
	v_lshrrev_b32_e32 v5, 1, v0
	v_and_b32_e32 v3, 15, v0
	v_writelane_b32 v254, s17, 31
	s_add_u32 s16, s24, 0x1200
	s_addc_u32 s17, s25, 0
	s_lshl_b32 s0, s0, 5
	s_and_b32 s0, s0, 0x60
	s_add_u32 s83, s2, 0x54800000
	s_addc_u32 s84, s3, 0
	s_add_u32 s18, s2, 0x58800000
	s_addc_u32 s19, s3, 0
	s_add_u32 s85, s2, 0x5a800000
	s_addc_u32 s86, s3, 0
	s_add_u32 s20, s2, 0x5c800000
	s_addc_u32 s21, s3, 0
	s_add_u32 s22, s2, 0x62800000
	s_addc_u32 s23, s3, 0
	s_add_u32 s26, s2, 0x62c00000
	s_addc_u32 s27, s3, 0
	s_add_u32 s34, s2, 0x5e800000
	v_and_b32_e32 v2, 3, v2
	v_and_b32_e32 v4, 2, v0
	v_and_b32_e32 v5, 4, v5
	s_addc_u32 s35, s3, 0
	v_bitop3_b32 v4, v5, v2, v4 bitop3:0x36
	v_lshl_or_b32 v174, s1, 6, v3
	s_add_u32 s36, s2, 0x100000
	v_lshlrev_b32_e32 v4, 4, v4
	v_lshlrev_b32_e32 v5, 7, v174
	v_or_b32_e32 v3, s0, v3
	s_addc_u32 s37, s3, 0
	v_or_b32_e32 v6, v5, v4
	v_lshlrev_b32_e32 v3, 7, v3
	v_bitop3_b32 v5, v5, 64, v4 bitop3:0x36
	s_cmpk_lt_u32 s14, 0x100
	v_or_b32_e32 v175, v3, v4
	v_bitop3_b32 v176, v3, 64, v4 bitop3:0x36
	v_add_u32_e32 v175, 0x10000, v175
	v_add_u32_e32 v176, 0x10000, v176
	s_cselect_b64 s[38:39], -1, 0
	v_lshl_or_b32 v177, v2, 3, s0
	v_mov_b64_e32 v[148:149], 0x53f
	s_add_i32 s87, 0, 0x10000
	s_add_i32 s88, 0, 0x10800
	s_add_i32 s89, 0, 0x14000
	s_add_i32 s90, 0, 0x14800
	v_add_u32_e32 v178, 0, v6
	v_add_u32_e32 v179, 0, v5
	s_add_i32 s92, 0, 0x18000
	s_add_i32 s93, 0, 0x18800
	s_add_i32 s94, 0, 0x1c000
	s_add_i32 s95, 0, 0x1c800
	s_mov_b32 s40, 0x3e000000
	s_mov_b32 s96, 0x40000
	s_mov_b32 s97, 0x48000
	s_mov_b32 s41, 0x50000
	s_mov_b32 s91, 0
	s_mov_b64 s[44:45], s[66:67]
	s_mov_b64 s[46:47], s[64:65]
	s_branch .LBB0_98
.Lp1_first:
	s_add_u32 s70, s64, s66
	s_addc_u32 s71, s65, s67
	s_add_u32 s73, s70, 0x100
	s_addc_u32 vcc_lo, s71, 0
	ds_read_b128 v[184:187], v175
	ds_read_b128 v[188:191], v176
	ds_read_b128 v[192:195], v175 offset:2048
	ds_read_b128 v[196:199], v176 offset:2048
	ds_read_b128 v[200:203], v175 offset:16384
	ds_read_b128 v[204:207], v176 offset:16384
	ds_read_b128 v[208:211], v175 offset:18432
	ds_read_b128 v[212:215], v176 offset:18432
	s_and_b64 s[70:71], s[68:69], exec
	s_cselect_b32 s71, s47, vcc_lo
	s_cselect_b32 s70, s46, s73
	s_add_u32 s73, s15, s66
	s_addc_u32 vcc_lo, s43, s67
	s_and_b64 s[68:69], s[68:69], exec
	s_cselect_b32 s69, s45, vcc_lo
	s_cselect_b32 s68, s44, s73
	v_lshl_add_u64 v[248:249], v[158:159], 0, s[66:67]
	s_add_i32 m0, s77, 0x8000
	ds_read_b128 v[216:219], v178
	ds_read_b128 v[220:223], v178 offset:2048
	ds_read_b128 v[224:227], v179
	ds_read_b128 v[228:231], v179 offset:2048
	ds_read_b128 v[232:235], v178 offset:4096
	ds_read_b128 v[236:239], v178 offset:6144
	ds_read_b128 v[240:243], v179 offset:4096
	ds_read_b128 v[244:247], v179 offset:6144
	global_load_lds_dwordx4 v[248:249], off
	v_lshl_add_u64 v[248:249], v[156:157], 0, s[66:67]
	s_add_i32 m0, s77, 0xa000
	s_nop 0
	global_load_lds_dwordx4 v[248:249], off
	v_lshl_add_u64 v[248:249], v[154:155], 0, s[66:67]
	s_add_i32 m0, s77, 0xc000
	s_nop 0
	global_load_lds_dwordx4 v[248:249], off
	v_lshl_add_u64 v[248:249], v[152:153], 0, s[66:67]
	s_add_i32 m0, s77, 0xe000
	s_nop 0
	global_load_lds_dwordx4 v[248:249], off
	s_waitcnt vmcnt(8)
	s_waitcnt lgkmcnt(0)
	s_barrier
	s_setprio 1
	s_waitcnt lgkmcnt(0)
	v_mfma_f32_16x16x32_bf16 v[126:129], v[184:187], v[216:219], 0
	v_mfma_f32_16x16x32_bf16 v[122:125], v[192:195], v[216:219], 0
	v_mfma_f32_16x16x32_bf16 v[118:121], v[184:187], v[220:223], 0
	v_mfma_f32_16x16x32_bf16 v[114:117], v[192:195], v[220:223], 0
	v_mfma_f32_16x16x32_bf16 v[110:113], v[184:187], v[232:235], 0
	v_mfma_f32_16x16x32_bf16 v[106:109], v[192:195], v[232:235], 0
	v_mfma_f32_16x16x32_bf16 v[102:105], v[184:187], v[236:239], 0
	v_mfma_f32_16x16x32_bf16 v[98:101], v[192:195], v[236:239], 0
	v_mfma_f32_16x16x32_bf16 v[126:129], v[188:191], v[224:227], v[126:129]
	v_mfma_f32_16x16x32_bf16 v[122:125], v[196:199], v[224:227], v[122:125]
	v_mfma_f32_16x16x32_bf16 v[118:121], v[188:191], v[228:231], v[118:121]
	v_mfma_f32_16x16x32_bf16 v[114:117], v[196:199], v[228:231], v[114:117]
	v_mfma_f32_16x16x32_bf16 v[110:113], v[188:191], v[240:243], v[110:113]
	v_mfma_f32_16x16x32_bf16 v[106:109], v[196:199], v[240:243], v[106:109]
	v_mfma_f32_16x16x32_bf16 v[102:105], v[188:191], v[244:247], v[102:105]
	v_mfma_f32_16x16x32_bf16 v[98:101], v[196:199], v[244:247], v[98:101]
	s_setprio 0
	s_setprio 1
	v_mfma_f32_16x16x32_bf16 v[62:65], v[200:203], v[216:219], 0
	v_mfma_f32_16x16x32_bf16 v[58:61], v[208:211], v[216:219], 0
	v_mfma_f32_16x16x32_bf16 v[54:57], v[200:203], v[220:223], 0
	v_mfma_f32_16x16x32_bf16 v[50:53], v[208:211], v[220:223], 0
	v_mfma_f32_16x16x32_bf16 v[46:49], v[200:203], v[232:235], 0
	v_mfma_f32_16x16x32_bf16 v[42:45], v[208:211], v[232:235], 0
	v_mfma_f32_16x16x32_bf16 v[38:41], v[200:203], v[236:239], 0
	v_mfma_f32_16x16x32_bf16 v[34:37], v[208:211], v[236:239], 0
	v_mfma_f32_16x16x32_bf16 v[62:65], v[204:207], v[224:227], v[62:65]
	v_mfma_f32_16x16x32_bf16 v[58:61], v[212:215], v[224:227], v[58:61]
	v_mfma_f32_16x16x32_bf16 v[54:57], v[204:207], v[228:231], v[54:57]
	v_mfma_f32_16x16x32_bf16 v[50:53], v[212:215], v[228:231], v[50:53]
	v_mfma_f32_16x16x32_bf16 v[46:49], v[204:207], v[240:243], v[46:49]
	v_mfma_f32_16x16x32_bf16 v[42:45], v[212:215], v[240:243], v[42:45]
	v_mfma_f32_16x16x32_bf16 v[38:41], v[204:207], v[244:247], v[38:41]
	v_mfma_f32_16x16x32_bf16 v[34:37], v[212:215], v[244:247], v[34:37]
	s_setprio 0
	s_barrier
	s_add_i32 s73, s87, s76
	v_lshl_add_u64 v[248:249], s[68:69], 0, v[142:143]
	s_mov_b32 m0, s73
	ds_read_b128 v[216:219], v178 offset:16384
	ds_read_b128 v[220:223], v178 offset:18432
	ds_read_b128 v[224:227], v179 offset:16384
	ds_read_b128 v[228:231], v179 offset:18432
	ds_read_b128 v[232:235], v178 offset:20480
	ds_read_b128 v[236:239], v178 offset:22528
	ds_read_b128 v[240:243], v179 offset:20480
	ds_read_b128 v[244:247], v179 offset:22528
	global_load_lds_dwordx4 v[248:249], off
	s_add_i32 m0, s73, 0x2000
	s_add_u32 vcc_lo, s68, 0x80000
	v_lshl_add_u64 v[250:251], s[68:69], 0, v[144:145]
	s_addc_u32 vcc_hi, s69, 0
	s_add_i32 s73, s89, s76
	global_load_lds_dwordx4 v[250:251], off
	v_lshl_add_u64 v[252:253], vcc, 0, v[142:143]
	s_mov_b32 m0, s73
	s_nop 0
	global_load_lds_dwordx4 v[252:253], off
	v_lshl_add_u64 v[252:253], vcc, 0, v[144:145]
	s_add_i32 m0, s73, 0x2000
	s_nop 0
	global_load_lds_dwordx4 v[252:253], off
	s_waitcnt vmcnt(6)
	s_waitcnt lgkmcnt(0)
	s_barrier
	s_setprio 1
	s_waitcnt lgkmcnt(0)
	v_mfma_f32_16x16x32_bf16 v[94:97], v[184:187], v[216:219], 0
	v_mfma_f32_16x16x32_bf16 v[90:93], v[192:195], v[216:219], 0
	v_mfma_f32_16x16x32_bf16 v[86:89], v[184:187], v[220:223], 0
	v_mfma_f32_16x16x32_bf16 v[82:85], v[192:195], v[220:223], 0
	v_mfma_f32_16x16x32_bf16 v[78:81], v[184:187], v[232:235], 0
	v_mfma_f32_16x16x32_bf16 v[74:77], v[192:195], v[232:235], 0
	v_mfma_f32_16x16x32_bf16 v[70:73], v[184:187], v[236:239], 0
	v_mfma_f32_16x16x32_bf16 v[66:69], v[192:195], v[236:239], 0
	v_mfma_f32_16x16x32_bf16 v[94:97], v[188:191], v[224:227], v[94:97]
	v_mfma_f32_16x16x32_bf16 v[90:93], v[196:199], v[224:227], v[90:93]
	v_mfma_f32_16x16x32_bf16 v[86:89], v[188:191], v[228:231], v[86:89]
	v_mfma_f32_16x16x32_bf16 v[82:85], v[196:199], v[228:231], v[82:85]
	v_mfma_f32_16x16x32_bf16 v[78:81], v[188:191], v[240:243], v[78:81]
	v_mfma_f32_16x16x32_bf16 v[74:77], v[196:199], v[240:243], v[74:77]
	v_mfma_f32_16x16x32_bf16 v[70:73], v[188:191], v[244:247], v[70:73]
	v_mfma_f32_16x16x32_bf16 v[66:69], v[196:199], v[244:247], v[66:69]
	s_setprio 0
	s_setprio 1
	v_mfma_f32_16x16x32_bf16 v[30:33], v[200:203], v[216:219], 0
	v_mfma_f32_16x16x32_bf16 v[26:29], v[208:211], v[216:219], 0
	v_mfma_f32_16x16x32_bf16 v[22:25], v[200:203], v[220:223], 0
	v_mfma_f32_16x16x32_bf16 v[18:21], v[208:211], v[220:223], 0
	v_mfma_f32_16x16x32_bf16 v[14:17], v[200:203], v[232:235], 0
	v_mfma_f32_16x16x32_bf16 v[10:13], v[208:211], v[232:235], 0
	v_mfma_f32_16x16x32_bf16 v[6:9], v[200:203], v[236:239], 0
	v_mfma_f32_16x16x32_bf16 v[2:5], v[208:211], v[236:239], 0
	v_mfma_f32_16x16x32_bf16 v[30:33], v[204:207], v[224:227], v[30:33]
	v_mfma_f32_16x16x32_bf16 v[26:29], v[212:215], v[224:227], v[26:29]
	v_mfma_f32_16x16x32_bf16 v[22:25], v[204:207], v[228:231], v[22:25]
	v_mfma_f32_16x16x32_bf16 v[18:21], v[212:215], v[228:231], v[18:21]
	v_mfma_f32_16x16x32_bf16 v[14:17], v[204:207], v[240:243], v[14:17]
	v_mfma_f32_16x16x32_bf16 v[10:13], v[212:215], v[240:243], v[10:13]
	v_mfma_f32_16x16x32_bf16 v[6:9], v[204:207], v[244:247], v[6:9]
	v_mfma_f32_16x16x32_bf16 v[2:5], v[212:215], v[244:247], v[2:5]
	s_setprio 0
	s_barrier
	s_branch .Lp1_blk3

.LBB0_101:
	s_cmp_eq_u32 s66, 0
	s_cbranch_scc1 .Lp1_first
	s_add_u32 s70, s64, s66
	s_addc_u32 s71, s65, s67
	s_add_u32 s73, s70, 0x100
	s_addc_u32 vcc_lo, s71, 0
	ds_read_b128 v[184:187], v175
	ds_read_b128 v[188:191], v176
	ds_read_b128 v[192:195], v175 offset:2048
	ds_read_b128 v[196:199], v176 offset:2048
	ds_read_b128 v[200:203], v175 offset:16384
	ds_read_b128 v[204:207], v176 offset:16384
	ds_read_b128 v[208:211], v175 offset:18432
	ds_read_b128 v[212:215], v176 offset:18432
	s_and_b64 s[70:71], s[68:69], exec
	s_cselect_b32 s71, s47, vcc_lo
	s_cselect_b32 s70, s46, s73
	s_add_u32 s73, s15, s66
	s_addc_u32 vcc_lo, s43, s67
	s_and_b64 s[68:69], s[68:69], exec
	s_cselect_b32 s69, s45, vcc_lo
	s_cselect_b32 s68, s44, s73
	v_lshl_add_u64 v[248:249], v[158:159], 0, s[66:67]
	s_add_i32 m0, s77, 0x8000
	ds_read_b128 v[216:219], v178
	ds_read_b128 v[220:223], v178 offset:2048
	ds_read_b128 v[224:227], v179
	ds_read_b128 v[228:231], v179 offset:2048
	ds_read_b128 v[232:235], v178 offset:4096
	ds_read_b128 v[236:239], v178 offset:6144
	ds_read_b128 v[240:243], v179 offset:4096
	ds_read_b128 v[244:247], v179 offset:6144
	global_load_lds_dwordx4 v[248:249], off
	v_lshl_add_u64 v[248:249], v[156:157], 0, s[66:67]
	s_add_i32 m0, s77, 0xa000
	s_nop 0
	global_load_lds_dwordx4 v[248:249], off
	v_lshl_add_u64 v[248:249], v[154:155], 0, s[66:67]
	s_add_i32 m0, s77, 0xc000
	s_nop 0
	global_load_lds_dwordx4 v[248:249], off
	v_lshl_add_u64 v[248:249], v[152:153], 0, s[66:67]
	s_add_i32 m0, s77, 0xe000
	s_nop 0
	global_load_lds_dwordx4 v[248:249], off
	s_waitcnt vmcnt(8)
	s_waitcnt lgkmcnt(0)
	s_barrier
	s_setprio 1
	s_waitcnt lgkmcnt(0)
	v_mfma_f32_16x16x32_bf16 v[126:129], v[184:187], v[216:219], v[126:129]
	v_mfma_f32_16x16x32_bf16 v[122:125], v[192:195], v[216:219], v[122:125]
	v_mfma_f32_16x16x32_bf16 v[118:121], v[184:187], v[220:223], v[118:121]
	v_mfma_f32_16x16x32_bf16 v[114:117], v[192:195], v[220:223], v[114:117]
	v_mfma_f32_16x16x32_bf16 v[110:113], v[184:187], v[232:235], v[110:113]
	v_mfma_f32_16x16x32_bf16 v[106:109], v[192:195], v[232:235], v[106:109]
	v_mfma_f32_16x16x32_bf16 v[102:105], v[184:187], v[236:239], v[102:105]
	v_mfma_f32_16x16x32_bf16 v[98:101], v[192:195], v[236:239], v[98:101]
	v_mfma_f32_16x16x32_bf16 v[126:129], v[188:191], v[224:227], v[126:129]
	v_mfma_f32_16x16x32_bf16 v[122:125], v[196:199], v[224:227], v[122:125]
	v_mfma_f32_16x16x32_bf16 v[118:121], v[188:191], v[228:231], v[118:121]
	v_mfma_f32_16x16x32_bf16 v[114:117], v[196:199], v[228:231], v[114:117]
	v_mfma_f32_16x16x32_bf16 v[110:113], v[188:191], v[240:243], v[110:113]
	v_mfma_f32_16x16x32_bf16 v[106:109], v[196:199], v[240:243], v[106:109]
	v_mfma_f32_16x16x32_bf16 v[102:105], v[188:191], v[244:247], v[102:105]
	v_mfma_f32_16x16x32_bf16 v[98:101], v[196:199], v[244:247], v[98:101]
	s_setprio 0
	s_setprio 1
	v_mfma_f32_16x16x32_bf16 v[62:65], v[200:203], v[216:219], v[62:65]
	v_mfma_f32_16x16x32_bf16 v[58:61], v[208:211], v[216:219], v[58:61]
	v_mfma_f32_16x16x32_bf16 v[54:57], v[200:203], v[220:223], v[54:57]
	v_mfma_f32_16x16x32_bf16 v[50:53], v[208:211], v[220:223], v[50:53]
	v_mfma_f32_16x16x32_bf16 v[46:49], v[200:203], v[232:235], v[46:49]
	v_mfma_f32_16x16x32_bf16 v[42:45], v[208:211], v[232:235], v[42:45]
	v_mfma_f32_16x16x32_bf16 v[38:41], v[200:203], v[236:239], v[38:41]
	v_mfma_f32_16x16x32_bf16 v[34:37], v[208:211], v[236:239], v[34:37]
	v_mfma_f32_16x16x32_bf16 v[62:65], v[204:207], v[224:227], v[62:65]
	v_mfma_f32_16x16x32_bf16 v[58:61], v[212:215], v[224:227], v[58:61]
	v_mfma_f32_16x16x32_bf16 v[54:57], v[204:207], v[228:231], v[54:57]
	v_mfma_f32_16x16x32_bf16 v[50:53], v[212:215], v[228:231], v[50:53]
	v_mfma_f32_16x16x32_bf16 v[46:49], v[204:207], v[240:243], v[46:49]
	v_mfma_f32_16x16x32_bf16 v[42:45], v[212:215], v[240:243], v[42:45]
	v_mfma_f32_16x16x32_bf16 v[38:41], v[204:207], v[244:247], v[38:41]
	v_mfma_f32_16x16x32_bf16 v[34:37], v[212:215], v[244:247], v[34:37]
	s_setprio 0
	s_barrier
	s_add_i32 s73, s87, s76
	v_lshl_add_u64 v[248:249], s[68:69], 0, v[142:143]
	s_mov_b32 m0, s73
	ds_read_b128 v[216:219], v178 offset:16384
	ds_read_b128 v[220:223], v178 offset:18432
	ds_read_b128 v[224:227], v179 offset:16384
	ds_read_b128 v[228:231], v179 offset:18432
	ds_read_b128 v[232:235], v178 offset:20480
	ds_read_b128 v[236:239], v178 offset:22528
	ds_read_b128 v[240:243], v179 offset:20480
	ds_read_b128 v[244:247], v179 offset:22528
	global_load_lds_dwordx4 v[248:249], off
	s_add_i32 m0, s73, 0x2000
	s_add_u32 vcc_lo, s68, 0x80000
	v_lshl_add_u64 v[250:251], s[68:69], 0, v[144:145]
	s_addc_u32 vcc_hi, s69, 0
	s_add_i32 s73, s89, s76
	global_load_lds_dwordx4 v[250:251], off
	v_lshl_add_u64 v[252:253], vcc, 0, v[142:143]
	s_mov_b32 m0, s73
	s_nop 0
	global_load_lds_dwordx4 v[252:253], off
	v_lshl_add_u64 v[252:253], vcc, 0, v[144:145]
	s_add_i32 m0, s73, 0x2000
	s_nop 0
	global_load_lds_dwordx4 v[252:253], off
	s_waitcnt vmcnt(6)
	s_waitcnt lgkmcnt(0)
	s_barrier
	s_setprio 1
	s_waitcnt lgkmcnt(0)
	v_mfma_f32_16x16x32_bf16 v[94:97], v[184:187], v[216:219], v[94:97]
	v_mfma_f32_16x16x32_bf16 v[90:93], v[192:195], v[216:219], v[90:93]
	v_mfma_f32_16x16x32_bf16 v[86:89], v[184:187], v[220:223], v[86:89]
	v_mfma_f32_16x16x32_bf16 v[82:85], v[192:195], v[220:223], v[82:85]
	v_mfma_f32_16x16x32_bf16 v[78:81], v[184:187], v[232:235], v[78:81]
	v_mfma_f32_16x16x32_bf16 v[74:77], v[192:195], v[232:235], v[74:77]
	v_mfma_f32_16x16x32_bf16 v[70:73], v[184:187], v[236:239], v[70:73]
	v_mfma_f32_16x16x32_bf16 v[66:69], v[192:195], v[236:239], v[66:69]
	v_mfma_f32_16x16x32_bf16 v[94:97], v[188:191], v[224:227], v[94:97]
	v_mfma_f32_16x16x32_bf16 v[90:93], v[196:199], v[224:227], v[90:93]
	v_mfma_f32_16x16x32_bf16 v[86:89], v[188:191], v[228:231], v[86:89]
	v_mfma_f32_16x16x32_bf16 v[82:85], v[196:199], v[228:231], v[82:85]
	v_mfma_f32_16x16x32_bf16 v[78:81], v[188:191], v[240:243], v[78:81]
	v_mfma_f32_16x16x32_bf16 v[74:77], v[196:199], v[240:243], v[74:77]
	v_mfma_f32_16x16x32_bf16 v[70:73], v[188:191], v[244:247], v[70:73]
	v_mfma_f32_16x16x32_bf16 v[66:69], v[196:199], v[244:247], v[66:69]
	s_setprio 0
	s_setprio 1
	v_mfma_f32_16x16x32_bf16 v[30:33], v[200:203], v[216:219], v[30:33]
	v_mfma_f32_16x16x32_bf16 v[26:29], v[208:211], v[216:219], v[26:29]
	v_mfma_f32_16x16x32_bf16 v[22:25], v[200:203], v[220:223], v[22:25]
	v_mfma_f32_16x16x32_bf16 v[18:21], v[208:211], v[220:223], v[18:21]
	v_mfma_f32_16x16x32_bf16 v[14:17], v[200:203], v[232:235], v[14:17]
	v_mfma_f32_16x16x32_bf16 v[10:13], v[208:211], v[232:235], v[10:13]
	v_mfma_f32_16x16x32_bf16 v[6:9], v[200:203], v[236:239], v[6:9]
	v_mfma_f32_16x16x32_bf16 v[2:5], v[208:211], v[236:239], v[2:5]
	v_mfma_f32_16x16x32_bf16 v[30:33], v[204:207], v[224:227], v[30:33]
	v_mfma_f32_16x16x32_bf16 v[26:29], v[212:215], v[224:227], v[26:29]
	v_mfma_f32_16x16x32_bf16 v[22:25], v[204:207], v[228:231], v[22:25]
	v_mfma_f32_16x16x32_bf16 v[18:21], v[212:215], v[228:231], v[18:21]
	v_mfma_f32_16x16x32_bf16 v[14:17], v[204:207], v[240:243], v[14:17]
	v_mfma_f32_16x16x32_bf16 v[10:13], v[212:215], v[240:243], v[10:13]
	v_mfma_f32_16x16x32_bf16 v[6:9], v[204:207], v[244:247], v[6:9]
	v_mfma_f32_16x16x32_bf16 v[2:5], v[212:215], v[244:247], v[2:5]
	s_setprio 0
	s_barrier
.Lp1_blk3:
	ds_read_b128 v[184:187], v175 offset:32768
	ds_read_b128 v[188:191], v176 offset:32768
	ds_read_b128 v[192:195], v175 offset:34816
	ds_read_b128 v[196:199], v176 offset:34816
	ds_read_b128 v[200:203], v175 offset:49152
	ds_read_b128 v[204:207], v176 offset:49152
	ds_read_b128 v[208:211], v175 offset:51200
	ds_read_b128 v[212:215], v176 offset:51200
	s_mov_b32 m0, s77
	v_lshl_add_u64 v[166:167], s[70:71], 0, v[166:167]
	ds_read_b128 v[216:219], v178 offset:32768
	ds_read_b128 v[220:223], v178 offset:34816
	ds_read_b128 v[224:227], v179 offset:32768
	ds_read_b128 v[228:231], v179 offset:34816
	ds_read_b128 v[232:235], v178 offset:36864
	ds_read_b128 v[236:239], v178 offset:38912
	ds_read_b128 v[240:243], v179 offset:36864
	ds_read_b128 v[244:247], v179 offset:38912
	global_load_lds_dwordx4 v[166:167], off
	v_lshl_add_u64 v[164:165], s[70:71], 0, v[164:165]
	s_mov_b32 m0, s78
	v_lshl_add_u64 v[162:163], s[70:71], 0, v[162:163]
	global_load_lds_dwordx4 v[164:165], off
	s_mov_b32 m0, s79
	v_lshl_add_u64 v[160:161], s[70:71], 0, v[160:161]
	global_load_lds_dwordx4 v[162:163], off
	s_mov_b32 m0, s80
	s_nop 0
	global_load_lds_dwordx4 v[160:161], off
	s_waitcnt vmcnt(8)
	s_waitcnt lgkmcnt(0)
	s_barrier
	s_setprio 1
	s_waitcnt lgkmcnt(0)
	v_mfma_f32_16x16x32_bf16 v[126:129], v[184:187], v[216:219], v[126:129]
	v_mfma_f32_16x16x32_bf16 v[122:125], v[192:195], v[216:219], v[122:125]
	v_mfma_f32_16x16x32_bf16 v[118:121], v[184:187], v[220:223], v[118:121]
	v_mfma_f32_16x16x32_bf16 v[114:117], v[192:195], v[220:223], v[114:117]
	v_mfma_f32_16x16x32_bf16 v[110:113], v[184:187], v[232:235], v[110:113]
	v_mfma_f32_16x16x32_bf16 v[106:109], v[192:195], v[232:235], v[106:109]
	v_mfma_f32_16x16x32_bf16 v[102:105], v[184:187], v[236:239], v[102:105]
	v_mfma_f32_16x16x32_bf16 v[98:101], v[192:195], v[236:239], v[98:101]
	v_mfma_f32_16x16x32_bf16 v[126:129], v[188:191], v[224:227], v[126:129]
	v_mfma_f32_16x16x32_bf16 v[122:125], v[196:199], v[224:227], v[122:125]
	v_mfma_f32_16x16x32_bf16 v[118:121], v[188:191], v[228:231], v[118:121]
	v_mfma_f32_16x16x32_bf16 v[114:117], v[196:199], v[228:231], v[114:117]
	v_mfma_f32_16x16x32_bf16 v[110:113], v[188:191], v[240:243], v[110:113]
	v_mfma_f32_16x16x32_bf16 v[106:109], v[196:199], v[240:243], v[106:109]
	v_mfma_f32_16x16x32_bf16 v[102:105], v[188:191], v[244:247], v[102:105]
	v_mfma_f32_16x16x32_bf16 v[98:101], v[196:199], v[244:247], v[98:101]
	s_setprio 0
	s_setprio 1
	v_mfma_f32_16x16x32_bf16 v[62:65], v[200:203], v[216:219], v[62:65]
	v_mfma_f32_16x16x32_bf16 v[58:61], v[208:211], v[216:219], v[58:61]
	v_mfma_f32_16x16x32_bf16 v[54:57], v[200:203], v[220:223], v[54:57]
	v_mfma_f32_16x16x32_bf16 v[50:53], v[208:211], v[220:223], v[50:53]
	v_mfma_f32_16x16x32_bf16 v[46:49], v[200:203], v[232:235], v[46:49]
	v_mfma_f32_16x16x32_bf16 v[42:45], v[208:211], v[232:235], v[42:45]
	v_mfma_f32_16x16x32_bf16 v[38:41], v[200:203], v[236:239], v[38:41]
	v_mfma_f32_16x16x32_bf16 v[34:37], v[208:211], v[236:239], v[34:37]
	v_mfma_f32_16x16x32_bf16 v[62:65], v[204:207], v[224:227], v[62:65]
	v_mfma_f32_16x16x32_bf16 v[58:61], v[212:215], v[224:227], v[58:61]
	v_mfma_f32_16x16x32_bf16 v[54:57], v[204:207], v[228:231], v[54:57]
	v_mfma_f32_16x16x32_bf16 v[50:53], v[212:215], v[228:231], v[50:53]
	v_mfma_f32_16x16x32_bf16 v[46:49], v[204:207], v[240:243], v[46:49]
	v_mfma_f32_16x16x32_bf16 v[42:45], v[212:215], v[240:243], v[42:45]
	v_mfma_f32_16x16x32_bf16 v[38:41], v[204:207], v[244:247], v[38:41]
	v_mfma_f32_16x16x32_bf16 v[34:37], v[212:215], v[244:247], v[34:37]
	s_setprio 0
	s_barrier
	s_add_i32 s70, s92, s76
	v_lshl_add_u64 v[240:241], v[248:249], 0, s[8:9]
	s_mov_b32 m0, s70
	ds_read_b128 v[160:163], v178 offset:49152
	ds_read_b128 v[164:167], v178 offset:51200
	ds_read_b128 v[216:219], v179 offset:49152
	ds_read_b128 v[220:223], v179 offset:51200
	ds_read_b128 v[224:227], v178 offset:53248
	ds_read_b128 v[228:231], v178 offset:55296
	ds_read_b128 v[232:235], v179 offset:53248
	ds_read_b128 v[236:239], v179 offset:55296
	global_load_lds_dwordx4 v[240:241], off
	s_add_i32 m0, s70, 0x2000
	s_add_u32 s68, s68, 0x80080
	v_lshl_add_u64 v[240:241], v[250:251], 0, s[8:9]
	s_addc_u32 s69, s69, 0
	s_add_i32 s70, s94, s76
	global_load_lds_dwordx4 v[240:241], off
	v_lshl_add_u64 v[240:241], s[68:69], 0, v[142:143]
	s_mov_b32 m0, s70
	s_nop 0
	global_load_lds_dwordx4 v[240:241], off
	v_lshl_add_u64 v[240:241], s[68:69], 0, v[144:145]
	s_add_i32 m0, s70, 0x2000
	s_nop 0
	global_load_lds_dwordx4 v[240:241], off
	s_waitcnt vmcnt(6)
	s_waitcnt lgkmcnt(0)
	s_barrier
	s_setprio 1
	s_waitcnt lgkmcnt(0)
	v_mfma_f32_16x16x32_bf16 v[94:97], v[184:187], v[160:163], v[94:97]
	v_mfma_f32_16x16x32_bf16 v[90:93], v[192:195], v[160:163], v[90:93]
	v_mfma_f32_16x16x32_bf16 v[86:89], v[184:187], v[164:167], v[86:89]
	v_mfma_f32_16x16x32_bf16 v[82:85], v[192:195], v[164:167], v[82:85]
	v_mfma_f32_16x16x32_bf16 v[78:81], v[184:187], v[224:227], v[78:81]
	v_mfma_f32_16x16x32_bf16 v[74:77], v[192:195], v[224:227], v[74:77]
	v_mfma_f32_16x16x32_bf16 v[70:73], v[184:187], v[228:231], v[70:73]
	v_mfma_f32_16x16x32_bf16 v[66:69], v[192:195], v[228:231], v[66:69]
	v_mfma_f32_16x16x32_bf16 v[94:97], v[188:191], v[216:219], v[94:97]
	v_mfma_f32_16x16x32_bf16 v[90:93], v[196:199], v[216:219], v[90:93]
	v_mfma_f32_16x16x32_bf16 v[86:89], v[188:191], v[220:223], v[86:89]
	v_mfma_f32_16x16x32_bf16 v[82:85], v[196:199], v[220:223], v[82:85]
	v_mfma_f32_16x16x32_bf16 v[78:81], v[188:191], v[232:235], v[78:81]
	v_mfma_f32_16x16x32_bf16 v[74:77], v[196:199], v[232:235], v[74:77]
	v_mfma_f32_16x16x32_bf16 v[70:73], v[188:191], v[236:239], v[70:73]
	v_mfma_f32_16x16x32_bf16 v[66:69], v[196:199], v[236:239], v[66:69]
	s_setprio 0
	s_setprio 1
	v_mfma_f32_16x16x32_bf16 v[30:33], v[200:203], v[160:163], v[30:33]
	v_mfma_f32_16x16x32_bf16 v[26:29], v[208:211], v[160:163], v[26:29]
	v_mfma_f32_16x16x32_bf16 v[22:25], v[200:203], v[164:167], v[22:25]
	v_mfma_f32_16x16x32_bf16 v[18:21], v[208:211], v[164:167], v[18:21]
	v_mfma_f32_16x16x32_bf16 v[14:17], v[200:203], v[224:227], v[14:17]
	v_mfma_f32_16x16x32_bf16 v[10:13], v[208:211], v[224:227], v[10:13]
	v_mfma_f32_16x16x32_bf16 v[6:9], v[200:203], v[228:231], v[6:9]
	v_mfma_f32_16x16x32_bf16 v[2:5], v[208:211], v[228:231], v[2:5]
	v_mfma_f32_16x16x32_bf16 v[30:33], v[204:207], v[216:219], v[30:33]
	v_mfma_f32_16x16x32_bf16 v[26:29], v[212:215], v[216:219], v[26:29]
	v_mfma_f32_16x16x32_bf16 v[22:25], v[204:207], v[220:223], v[22:25]
	v_mfma_f32_16x16x32_bf16 v[18:21], v[212:215], v[220:223], v[18:21]
	v_mfma_f32_16x16x32_bf16 v[14:17], v[204:207], v[232:235], v[14:17]
	v_mfma_f32_16x16x32_bf16 v[10:13], v[212:215], v[232:235], v[10:13]
	v_mfma_f32_16x16x32_bf16 v[6:9], v[204:207], v[236:239], v[6:9]
	v_mfma_f32_16x16x32_bf16 v[2:5], v[212:215], v[236:239], v[2:5]
	s_setprio 0
	s_barrier
	s_add_i32 s72, s72, 2
	s_add_u32 s66, s66, 0x100
	s_addc_u32 s67, s67, 0
	s_cmp_gt_u32 s72, 29
	s_cbranch_scc1 .LBB0_105

.LBB0_375:
	s_sext_i32_i8 s74, s0
	s_lshl_b32 s0, s12, 5
	v_lshrrev_b32_e32 v5, 1, v0
	s_ashr_i32 s44, s94, 31
	s_and_b32 s0, s0, 0x60
	v_and_b32_e32 v3, 15, v0
	v_and_b32_e32 v2, 3, v2
	v_and_b32_e32 v4, 2, v0
	v_and_b32_e32 v5, 4, v5
	s_add_u32 s12, s2, 0x36800000
	v_bitop3_b32 v4, v5, v2, v4 bitop3:0x36
	v_lshl_or_b32 v173, s13, 6, v3
	s_addc_u32 s13, s3, 0
	v_lshlrev_b32_e32 v4, 4, v4
	v_lshlrev_b32_e32 v5, 7, v173
	v_or_b32_e32 v3, s0, v3
	s_cmpk_lt_u32 s1, 0x100
	v_or_b32_e32 v6, v5, v4
	v_lshlrev_b32_e32 v3, 7, v3
	v_bitop3_b32 v5, v5, 64, v4 bitop3:0x36
	s_cselect_b64 s[14:15], -1, 0
	s_add_u32 s16, s2, 0x63000080
	v_or_b32_e32 v174, v3, v4
	v_bitop3_b32 v175, v3, 64, v4 bitop3:0x36
	v_add_u32_e32 v174, 0x10000, v174
	v_add_u32_e32 v175, 0x10000, v175
	v_lshl_or_b32 v176, v2, 3, s0
	s_addc_u32 s17, s3, 0
	v_mov_b64_e32 v[152:153], 0x1ff
	s_add_i32 s45, 0, 0x10000
	s_add_i32 s46, 0, 0x10800
	s_add_i32 s47, 0, 0x14000
	s_add_i32 s64, 0, 0x14800
	v_add_u32_e32 v177, 0, v6
	v_add_u32_e32 v178, 0, v5
	s_add_i32 s65, 0, 0x18000
	s_add_i32 s66, 0, 0x18800
	s_add_i32 s67, 0, 0x1c000
	s_add_i32 s68, 0, 0x1c800
	s_mov_b64 s[18:19], 0x90000
	s_mov_b32 s69, 0x90000
	s_mov_b64 s[20:21], 0xa0000
	s_mov_b32 s70, 0xa0000
	s_mov_b64 s[22:23], 0xb0000
	s_mov_b32 s71, 0xb0000
	s_mov_b64 s[26:27], s[28:29]
	s_branch .LBB0_378
.Lp3_first:
	s_add_u32 s34, s2, s28
	ds_read_b128 v[184:187], v174
	ds_read_b128 v[188:191], v175
	s_addc_u32 s35, s3, s29
	ds_read_b128 v[192:195], v174 offset:2048
	ds_read_b128 v[196:199], v175 offset:2048
	s_add_u32 s77, s34, 0x63000100
	ds_read_b128 v[200:203], v174 offset:16384
	ds_read_b128 v[204:207], v175 offset:16384
	s_addc_u32 s78, s35, 0
	ds_read_b128 v[208:211], v174 offset:18432
	ds_read_b128 v[212:215], v175 offset:18432
	s_and_b64 s[34:35], s[30:31], exec
	s_cselect_b32 s35, s7, s78
	s_cselect_b32 s34, s6, s77
	s_add_u32 s77, s25, s28
	s_addc_u32 s78, s75, s29
	s_and_b64 s[30:31], s[30:31], exec
	s_cselect_b32 s31, s27, s78
	s_cselect_b32 s30, s26, s77
	v_lshl_add_u64 v[248:249], v[158:159], 0, s[28:29]
	s_add_i32 m0, s39, 0x8000
	ds_read_b128 v[216:219], v177
	ds_read_b128 v[220:223], v177 offset:2048
	ds_read_b128 v[224:227], v178
	ds_read_b128 v[228:231], v178 offset:2048
	ds_read_b128 v[232:235], v177 offset:4096
	ds_read_b128 v[236:239], v177 offset:6144
	ds_read_b128 v[240:243], v178 offset:4096
	ds_read_b128 v[244:247], v178 offset:6144
	global_load_lds_dwordx4 v[248:249], off
	v_lshl_add_u64 v[248:249], v[156:157], 0, s[28:29]
	s_add_i32 m0, s39, 0xa000
	s_nop 0
	global_load_lds_dwordx4 v[248:249], off
	v_lshl_add_u64 v[248:249], v[154:155], 0, s[28:29]
	s_add_i32 m0, s39, 0xc000
	s_nop 0
	global_load_lds_dwordx4 v[248:249], off
	v_lshl_add_u64 v[248:249], v[144:145], 0, s[28:29]
	s_add_i32 m0, s39, 0xe000
	s_nop 0
	global_load_lds_dwordx4 v[248:249], off
	s_waitcnt vmcnt(8)
	s_waitcnt lgkmcnt(0)
	s_barrier
	s_setprio 1
	s_waitcnt lgkmcnt(0)
	v_mfma_f32_16x16x32_bf16 v[126:129], v[184:187], v[216:219], 0
	v_mfma_f32_16x16x32_bf16 v[122:125], v[192:195], v[216:219], 0
	v_mfma_f32_16x16x32_bf16 v[118:121], v[184:187], v[220:223], 0
	v_mfma_f32_16x16x32_bf16 v[114:117], v[192:195], v[220:223], 0
	v_mfma_f32_16x16x32_bf16 v[110:113], v[184:187], v[232:235], 0
	v_mfma_f32_16x16x32_bf16 v[102:105], v[192:195], v[232:235], 0
	v_mfma_f32_16x16x32_bf16 v[94:97], v[184:187], v[236:239], 0
	v_mfma_f32_16x16x32_bf16 v[86:89], v[192:195], v[236:239], 0
	v_mfma_f32_16x16x32_bf16 v[126:129], v[188:191], v[224:227], v[126:129]
	v_mfma_f32_16x16x32_bf16 v[122:125], v[196:199], v[224:227], v[122:125]
	v_mfma_f32_16x16x32_bf16 v[118:121], v[188:191], v[228:231], v[118:121]
	v_mfma_f32_16x16x32_bf16 v[114:117], v[196:199], v[228:231], v[114:117]
	v_mfma_f32_16x16x32_bf16 v[110:113], v[188:191], v[240:243], v[110:113]
	v_mfma_f32_16x16x32_bf16 v[102:105], v[196:199], v[240:243], v[102:105]
	v_mfma_f32_16x16x32_bf16 v[94:97], v[188:191], v[244:247], v[94:97]
	v_mfma_f32_16x16x32_bf16 v[86:89], v[196:199], v[244:247], v[86:89]
	s_setprio 0
	s_setprio 1
	v_mfma_f32_16x16x32_bf16 v[106:109], v[200:203], v[216:219], 0
	v_mfma_f32_16x16x32_bf16 v[98:101], v[208:211], v[216:219], 0
	v_mfma_f32_16x16x32_bf16 v[90:93], v[200:203], v[220:223], 0
	v_mfma_f32_16x16x32_bf16 v[82:85], v[208:211], v[220:223], 0
	v_mfma_f32_16x16x32_bf16 v[78:81], v[200:203], v[232:235], 0
	v_mfma_f32_16x16x32_bf16 v[74:77], v[208:211], v[232:235], 0
	v_mfma_f32_16x16x32_bf16 v[70:73], v[200:203], v[236:239], 0
	v_mfma_f32_16x16x32_bf16 v[66:69], v[208:211], v[236:239], 0
	v_mfma_f32_16x16x32_bf16 v[106:109], v[204:207], v[224:227], v[106:109]
	v_mfma_f32_16x16x32_bf16 v[98:101], v[212:215], v[224:227], v[98:101]
	v_mfma_f32_16x16x32_bf16 v[90:93], v[204:207], v[228:231], v[90:93]
	v_mfma_f32_16x16x32_bf16 v[82:85], v[212:215], v[228:231], v[82:85]
	v_mfma_f32_16x16x32_bf16 v[78:81], v[204:207], v[240:243], v[78:81]
	v_mfma_f32_16x16x32_bf16 v[74:77], v[212:215], v[240:243], v[74:77]
	v_mfma_f32_16x16x32_bf16 v[70:73], v[204:207], v[244:247], v[70:73]
	v_mfma_f32_16x16x32_bf16 v[66:69], v[212:215], v[244:247], v[66:69]
	s_setprio 0
	s_barrier
	s_add_i32 s77, s45, s33
	v_lshl_add_u64 v[248:249], s[30:31], 0, v[146:147]
	s_mov_b32 m0, s77
	ds_read_b128 v[216:219], v177 offset:16384
	ds_read_b128 v[220:223], v177 offset:18432
	ds_read_b128 v[224:227], v178 offset:16384
	ds_read_b128 v[228:231], v178 offset:18432
	ds_read_b128 v[232:235], v177 offset:20480
	ds_read_b128 v[236:239], v177 offset:22528
	ds_read_b128 v[240:243], v178 offset:20480
	ds_read_b128 v[244:247], v178 offset:22528
	global_load_lds_dwordx4 v[248:249], off
	s_add_i32 m0, s77, 0x2000
	s_add_u32 s78, s30, 0x80000
	v_lshl_add_u64 v[250:251], s[30:31], 0, v[148:149]
	s_addc_u32 s79, s31, 0
	s_add_i32 s77, s47, s33
	global_load_lds_dwordx4 v[250:251], off
	v_lshl_add_u64 v[252:253], s[78:79], 0, v[146:147]
	s_mov_b32 m0, s77
	s_nop 0
	global_load_lds_dwordx4 v[252:253], off
	v_lshl_add_u64 v[252:253], s[78:79], 0, v[148:149]
	s_add_i32 m0, s77, 0x2000
	s_nop 0
	global_load_lds_dwordx4 v[252:253], off
	s_waitcnt vmcnt(6)
	s_waitcnt lgkmcnt(0)
	s_barrier
	s_setprio 1
	s_waitcnt lgkmcnt(0)
	v_mfma_f32_16x16x32_bf16 v[62:65], v[184:187], v[216:219], 0
	v_mfma_f32_16x16x32_bf16 v[58:61], v[192:195], v[216:219], 0
	v_mfma_f32_16x16x32_bf16 v[50:53], v[184:187], v[220:223], 0
	v_mfma_f32_16x16x32_bf16 v[42:45], v[192:195], v[220:223], 0
	v_mfma_f32_16x16x32_bf16 v[34:37], v[184:187], v[232:235], 0
	v_mfma_f32_16x16x32_bf16 v[26:29], v[192:195], v[232:235], 0
	v_mfma_f32_16x16x32_bf16 v[18:21], v[184:187], v[236:239], 0
	v_mfma_f32_16x16x32_bf16 v[10:13], v[192:195], v[236:239], 0
	v_mfma_f32_16x16x32_bf16 v[62:65], v[188:191], v[224:227], v[62:65]
	v_mfma_f32_16x16x32_bf16 v[58:61], v[196:199], v[224:227], v[58:61]
	v_mfma_f32_16x16x32_bf16 v[50:53], v[188:191], v[228:231], v[50:53]
	v_mfma_f32_16x16x32_bf16 v[42:45], v[196:199], v[228:231], v[42:45]
	v_mfma_f32_16x16x32_bf16 v[34:37], v[188:191], v[240:243], v[34:37]
	v_mfma_f32_16x16x32_bf16 v[26:29], v[196:199], v[240:243], v[26:29]
	v_mfma_f32_16x16x32_bf16 v[18:21], v[188:191], v[244:247], v[18:21]
	v_mfma_f32_16x16x32_bf16 v[10:13], v[196:199], v[244:247], v[10:13]
	s_setprio 0
	s_setprio 1
	v_mfma_f32_16x16x32_bf16 v[54:57], v[200:203], v[216:219], 0
	v_mfma_f32_16x16x32_bf16 v[46:49], v[208:211], v[216:219], 0
	v_mfma_f32_16x16x32_bf16 v[38:41], v[200:203], v[220:223], 0
	v_mfma_f32_16x16x32_bf16 v[30:33], v[208:211], v[220:223], 0
	v_mfma_f32_16x16x32_bf16 v[22:25], v[200:203], v[232:235], 0
	v_mfma_f32_16x16x32_bf16 v[14:17], v[208:211], v[232:235], 0
	v_mfma_f32_16x16x32_bf16 v[6:9], v[200:203], v[236:239], 0
	v_mfma_f32_16x16x32_bf16 v[2:5], v[208:211], v[236:239], 0
	v_mfma_f32_16x16x32_bf16 v[54:57], v[204:207], v[224:227], v[54:57]
	v_mfma_f32_16x16x32_bf16 v[46:49], v[212:215], v[224:227], v[46:49]
	v_mfma_f32_16x16x32_bf16 v[38:41], v[204:207], v[228:231], v[38:41]
	v_mfma_f32_16x16x32_bf16 v[30:33], v[212:215], v[228:231], v[30:33]
	v_mfma_f32_16x16x32_bf16 v[22:25], v[204:207], v[240:243], v[22:25]
	v_mfma_f32_16x16x32_bf16 v[14:17], v[212:215], v[240:243], v[14:17]
	v_mfma_f32_16x16x32_bf16 v[6:9], v[204:207], v[244:247], v[6:9]
	v_mfma_f32_16x16x32_bf16 v[2:5], v[212:215], v[244:247], v[2:5]
	s_setprio 0
	s_barrier
	s_branch .Lp3_blk3

.LBB0_385:
	s_cmp_eq_u32 s28, 0
	s_cbranch_scc1 .Lp3_first
	s_add_u32 s34, s2, s28
	ds_read_b128 v[184:187], v174
	ds_read_b128 v[188:191], v175
	s_addc_u32 s35, s3, s29
	ds_read_b128 v[192:195], v174 offset:2048
	ds_read_b128 v[196:199], v175 offset:2048
	s_add_u32 s77, s34, 0x63000100
	ds_read_b128 v[200:203], v174 offset:16384
	ds_read_b128 v[204:207], v175 offset:16384
	s_addc_u32 s78, s35, 0
	ds_read_b128 v[208:211], v174 offset:18432
	ds_read_b128 v[212:215], v175 offset:18432
	s_and_b64 s[34:35], s[30:31], exec
	s_cselect_b32 s35, s7, s78
	s_cselect_b32 s34, s6, s77
	s_add_u32 s77, s25, s28
	s_addc_u32 s78, s75, s29
	s_and_b64 s[30:31], s[30:31], exec
	s_cselect_b32 s31, s27, s78
	s_cselect_b32 s30, s26, s77
	v_lshl_add_u64 v[248:249], v[158:159], 0, s[28:29]
	s_add_i32 m0, s39, 0x8000
	ds_read_b128 v[216:219], v177
	ds_read_b128 v[220:223], v177 offset:2048
	ds_read_b128 v[224:227], v178
	ds_read_b128 v[228:231], v178 offset:2048
	ds_read_b128 v[232:235], v177 offset:4096
	ds_read_b128 v[236:239], v177 offset:6144
	ds_read_b128 v[240:243], v178 offset:4096
	ds_read_b128 v[244:247], v178 offset:6144
	global_load_lds_dwordx4 v[248:249], off
	v_lshl_add_u64 v[248:249], v[156:157], 0, s[28:29]
	s_add_i32 m0, s39, 0xa000
	s_nop 0
	global_load_lds_dwordx4 v[248:249], off
	v_lshl_add_u64 v[248:249], v[154:155], 0, s[28:29]
	s_add_i32 m0, s39, 0xc000
	s_nop 0
	global_load_lds_dwordx4 v[248:249], off
	v_lshl_add_u64 v[248:249], v[144:145], 0, s[28:29]
	s_add_i32 m0, s39, 0xe000
	s_nop 0
	global_load_lds_dwordx4 v[248:249], off
	s_waitcnt vmcnt(8)
	s_waitcnt lgkmcnt(0)
	s_barrier
	s_setprio 1
	s_waitcnt lgkmcnt(0)
	v_mfma_f32_16x16x32_bf16 v[126:129], v[184:187], v[216:219], v[126:129]
	v_mfma_f32_16x16x32_bf16 v[122:125], v[192:195], v[216:219], v[122:125]
	v_mfma_f32_16x16x32_bf16 v[118:121], v[184:187], v[220:223], v[118:121]
	v_mfma_f32_16x16x32_bf16 v[114:117], v[192:195], v[220:223], v[114:117]
	v_mfma_f32_16x16x32_bf16 v[110:113], v[184:187], v[232:235], v[110:113]
	v_mfma_f32_16x16x32_bf16 v[102:105], v[192:195], v[232:235], v[102:105]
	v_mfma_f32_16x16x32_bf16 v[94:97], v[184:187], v[236:239], v[94:97]
	v_mfma_f32_16x16x32_bf16 v[86:89], v[192:195], v[236:239], v[86:89]
	v_mfma_f32_16x16x32_bf16 v[126:129], v[188:191], v[224:227], v[126:129]
	v_mfma_f32_16x16x32_bf16 v[122:125], v[196:199], v[224:227], v[122:125]
	v_mfma_f32_16x16x32_bf16 v[118:121], v[188:191], v[228:231], v[118:121]
	v_mfma_f32_16x16x32_bf16 v[114:117], v[196:199], v[228:231], v[114:117]
	v_mfma_f32_16x16x32_bf16 v[110:113], v[188:191], v[240:243], v[110:113]
	v_mfma_f32_16x16x32_bf16 v[102:105], v[196:199], v[240:243], v[102:105]
	v_mfma_f32_16x16x32_bf16 v[94:97], v[188:191], v[244:247], v[94:97]
	v_mfma_f32_16x16x32_bf16 v[86:89], v[196:199], v[244:247], v[86:89]
	s_setprio 0
	s_setprio 1
	v_mfma_f32_16x16x32_bf16 v[106:109], v[200:203], v[216:219], v[106:109]
	v_mfma_f32_16x16x32_bf16 v[98:101], v[208:211], v[216:219], v[98:101]
	v_mfma_f32_16x16x32_bf16 v[90:93], v[200:203], v[220:223], v[90:93]
	v_mfma_f32_16x16x32_bf16 v[82:85], v[208:211], v[220:223], v[82:85]
	v_mfma_f32_16x16x32_bf16 v[78:81], v[200:203], v[232:235], v[78:81]
	v_mfma_f32_16x16x32_bf16 v[74:77], v[208:211], v[232:235], v[74:77]
	v_mfma_f32_16x16x32_bf16 v[70:73], v[200:203], v[236:239], v[70:73]
	v_mfma_f32_16x16x32_bf16 v[66:69], v[208:211], v[236:239], v[66:69]
	v_mfma_f32_16x16x32_bf16 v[106:109], v[204:207], v[224:227], v[106:109]
	v_mfma_f32_16x16x32_bf16 v[98:101], v[212:215], v[224:227], v[98:101]
	v_mfma_f32_16x16x32_bf16 v[90:93], v[204:207], v[228:231], v[90:93]
	v_mfma_f32_16x16x32_bf16 v[82:85], v[212:215], v[228:231], v[82:85]
	v_mfma_f32_16x16x32_bf16 v[78:81], v[204:207], v[240:243], v[78:81]
	v_mfma_f32_16x16x32_bf16 v[74:77], v[212:215], v[240:243], v[74:77]
	v_mfma_f32_16x16x32_bf16 v[70:73], v[204:207], v[244:247], v[70:73]
	v_mfma_f32_16x16x32_bf16 v[66:69], v[212:215], v[244:247], v[66:69]
	s_setprio 0
	s_barrier
	s_add_i32 s77, s45, s33
	v_lshl_add_u64 v[248:249], s[30:31], 0, v[146:147]
	s_mov_b32 m0, s77
	ds_read_b128 v[216:219], v177 offset:16384
	ds_read_b128 v[220:223], v177 offset:18432
	ds_read_b128 v[224:227], v178 offset:16384
	ds_read_b128 v[228:231], v178 offset:18432
	ds_read_b128 v[232:235], v177 offset:20480
	ds_read_b128 v[236:239], v177 offset:22528
	ds_read_b128 v[240:243], v178 offset:20480
	ds_read_b128 v[244:247], v178 offset:22528
	global_load_lds_dwordx4 v[248:249], off
	s_add_i32 m0, s77, 0x2000
	s_add_u32 s78, s30, 0x80000
	v_lshl_add_u64 v[250:251], s[30:31], 0, v[148:149]
	s_addc_u32 s79, s31, 0
	s_add_i32 s77, s47, s33
	global_load_lds_dwordx4 v[250:251], off
	v_lshl_add_u64 v[252:253], s[78:79], 0, v[146:147]
	s_mov_b32 m0, s77
	s_nop 0
	global_load_lds_dwordx4 v[252:253], off
	v_lshl_add_u64 v[252:253], s[78:79], 0, v[148:149]
	s_add_i32 m0, s77, 0x2000
	s_nop 0
	global_load_lds_dwordx4 v[252:253], off
	s_waitcnt vmcnt(6)
	s_waitcnt lgkmcnt(0)
	s_barrier
	s_setprio 1
	s_waitcnt lgkmcnt(0)
	v_mfma_f32_16x16x32_bf16 v[62:65], v[184:187], v[216:219], v[62:65]
	v_mfma_f32_16x16x32_bf16 v[58:61], v[192:195], v[216:219], v[58:61]
	v_mfma_f32_16x16x32_bf16 v[50:53], v[184:187], v[220:223], v[50:53]
	v_mfma_f32_16x16x32_bf16 v[42:45], v[192:195], v[220:223], v[42:45]
	v_mfma_f32_16x16x32_bf16 v[34:37], v[184:187], v[232:235], v[34:37]
	v_mfma_f32_16x16x32_bf16 v[26:29], v[192:195], v[232:235], v[26:29]
	v_mfma_f32_16x16x32_bf16 v[18:21], v[184:187], v[236:239], v[18:21]
	v_mfma_f32_16x16x32_bf16 v[10:13], v[192:195], v[236:239], v[10:13]
	v_mfma_f32_16x16x32_bf16 v[62:65], v[188:191], v[224:227], v[62:65]
	v_mfma_f32_16x16x32_bf16 v[58:61], v[196:199], v[224:227], v[58:61]
	v_mfma_f32_16x16x32_bf16 v[50:53], v[188:191], v[228:231], v[50:53]
	v_mfma_f32_16x16x32_bf16 v[42:45], v[196:199], v[228:231], v[42:45]
	v_mfma_f32_16x16x32_bf16 v[34:37], v[188:191], v[240:243], v[34:37]
	v_mfma_f32_16x16x32_bf16 v[26:29], v[196:199], v[240:243], v[26:29]
	v_mfma_f32_16x16x32_bf16 v[18:21], v[188:191], v[244:247], v[18:21]
	v_mfma_f32_16x16x32_bf16 v[10:13], v[196:199], v[244:247], v[10:13]
	s_setprio 0
	s_setprio 1
	v_mfma_f32_16x16x32_bf16 v[54:57], v[200:203], v[216:219], v[54:57]
	v_mfma_f32_16x16x32_bf16 v[46:49], v[208:211], v[216:219], v[46:49]
	v_mfma_f32_16x16x32_bf16 v[38:41], v[200:203], v[220:223], v[38:41]
	v_mfma_f32_16x16x32_bf16 v[30:33], v[208:211], v[220:223], v[30:33]
	v_mfma_f32_16x16x32_bf16 v[22:25], v[200:203], v[232:235], v[22:25]
	v_mfma_f32_16x16x32_bf16 v[14:17], v[208:211], v[232:235], v[14:17]
	v_mfma_f32_16x16x32_bf16 v[6:9], v[200:203], v[236:239], v[6:9]
	v_mfma_f32_16x16x32_bf16 v[2:5], v[208:211], v[236:239], v[2:5]
	v_mfma_f32_16x16x32_bf16 v[54:57], v[204:207], v[224:227], v[54:57]
	v_mfma_f32_16x16x32_bf16 v[46:49], v[212:215], v[224:227], v[46:49]
	v_mfma_f32_16x16x32_bf16 v[38:41], v[204:207], v[228:231], v[38:41]
	v_mfma_f32_16x16x32_bf16 v[30:33], v[212:215], v[228:231], v[30:33]
	v_mfma_f32_16x16x32_bf16 v[22:25], v[204:207], v[240:243], v[22:25]
	v_mfma_f32_16x16x32_bf16 v[14:17], v[212:215], v[240:243], v[14:17]
	v_mfma_f32_16x16x32_bf16 v[6:9], v[204:207], v[244:247], v[6:9]
	v_mfma_f32_16x16x32_bf16 v[2:5], v[212:215], v[244:247], v[2:5]
	s_setprio 0
	s_barrier
.Lp3_blk3:
	ds_read_b128 v[184:187], v174 offset:32768
	ds_read_b128 v[188:191], v175 offset:32768
	ds_read_b128 v[192:195], v174 offset:34816
	ds_read_b128 v[196:199], v175 offset:34816
	ds_read_b128 v[200:203], v174 offset:49152
	ds_read_b128 v[204:207], v175 offset:49152
	ds_read_b128 v[208:211], v174 offset:51200
	ds_read_b128 v[212:215], v175 offset:51200
	s_mov_b32 m0, s39
	v_lshl_add_u64 v[166:167], s[34:35], 0, v[166:167]
	ds_read_b128 v[216:219], v177 offset:32768
	ds_read_b128 v[220:223], v177 offset:34816
	ds_read_b128 v[224:227], v178 offset:32768
	ds_read_b128 v[228:231], v178 offset:34816
	ds_read_b128 v[232:235], v177 offset:36864
	ds_read_b128 v[236:239], v177 offset:38912
	ds_read_b128 v[240:243], v178 offset:36864
	ds_read_b128 v[244:247], v178 offset:38912
	global_load_lds_dwordx4 v[166:167], off
	v_lshl_add_u64 v[164:165], s[34:35], 0, v[164:165]
	s_mov_b32 m0, s40
	v_lshl_add_u64 v[162:163], s[34:35], 0, v[162:163]
	global_load_lds_dwordx4 v[164:165], off
	s_mov_b32 m0, s41
	v_lshl_add_u64 v[160:161], s[34:35], 0, v[160:161]
	global_load_lds_dwordx4 v[162:163], off
	s_mov_b32 m0, s42
	s_nop 0
	global_load_lds_dwordx4 v[160:161], off
	s_waitcnt vmcnt(8)
	s_waitcnt lgkmcnt(0)
	s_barrier
	s_setprio 1
	s_waitcnt lgkmcnt(0)
	v_mfma_f32_16x16x32_bf16 v[126:129], v[184:187], v[216:219], v[126:129]
	v_mfma_f32_16x16x32_bf16 v[122:125], v[192:195], v[216:219], v[122:125]
	v_mfma_f32_16x16x32_bf16 v[118:121], v[184:187], v[220:223], v[118:121]
	v_mfma_f32_16x16x32_bf16 v[114:117], v[192:195], v[220:223], v[114:117]
	v_mfma_f32_16x16x32_bf16 v[110:113], v[184:187], v[232:235], v[110:113]
	v_mfma_f32_16x16x32_bf16 v[102:105], v[192:195], v[232:235], v[102:105]
	v_mfma_f32_16x16x32_bf16 v[94:97], v[184:187], v[236:239], v[94:97]
	v_mfma_f32_16x16x32_bf16 v[86:89], v[192:195], v[236:239], v[86:89]
	v_mfma_f32_16x16x32_bf16 v[126:129], v[188:191], v[224:227], v[126:129]
	v_mfma_f32_16x16x32_bf16 v[122:125], v[196:199], v[224:227], v[122:125]
	v_mfma_f32_16x16x32_bf16 v[118:121], v[188:191], v[228:231], v[118:121]
	v_mfma_f32_16x16x32_bf16 v[114:117], v[196:199], v[228:231], v[114:117]
	v_mfma_f32_16x16x32_bf16 v[110:113], v[188:191], v[240:243], v[110:113]
	v_mfma_f32_16x16x32_bf16 v[102:105], v[196:199], v[240:243], v[102:105]
	v_mfma_f32_16x16x32_bf16 v[94:97], v[188:191], v[244:247], v[94:97]
	v_mfma_f32_16x16x32_bf16 v[86:89], v[196:199], v[244:247], v[86:89]
	s_setprio 0
	s_setprio 1
	v_mfma_f32_16x16x32_bf16 v[106:109], v[200:203], v[216:219], v[106:109]
	v_mfma_f32_16x16x32_bf16 v[98:101], v[208:211], v[216:219], v[98:101]
	v_mfma_f32_16x16x32_bf16 v[90:93], v[200:203], v[220:223], v[90:93]
	v_mfma_f32_16x16x32_bf16 v[82:85], v[208:211], v[220:223], v[82:85]
	v_mfma_f32_16x16x32_bf16 v[78:81], v[200:203], v[232:235], v[78:81]
	v_mfma_f32_16x16x32_bf16 v[74:77], v[208:211], v[232:235], v[74:77]
	v_mfma_f32_16x16x32_bf16 v[70:73], v[200:203], v[236:239], v[70:73]
	v_mfma_f32_16x16x32_bf16 v[66:69], v[208:211], v[236:239], v[66:69]
	v_mfma_f32_16x16x32_bf16 v[106:109], v[204:207], v[224:227], v[106:109]
	v_mfma_f32_16x16x32_bf16 v[98:101], v[212:215], v[224:227], v[98:101]
	v_mfma_f32_16x16x32_bf16 v[90:93], v[204:207], v[228:231], v[90:93]
	v_mfma_f32_16x16x32_bf16 v[82:85], v[212:215], v[228:231], v[82:85]
	v_mfma_f32_16x16x32_bf16 v[78:81], v[204:207], v[240:243], v[78:81]
	v_mfma_f32_16x16x32_bf16 v[74:77], v[212:215], v[240:243], v[74:77]
	v_mfma_f32_16x16x32_bf16 v[70:73], v[204:207], v[244:247], v[70:73]
	v_mfma_f32_16x16x32_bf16 v[66:69], v[212:215], v[244:247], v[66:69]
	s_setprio 0
	s_barrier
	s_add_i32 s34, s65, s33
	v_lshl_add_u64 v[240:241], v[248:249], 0, s[8:9]
	s_mov_b32 m0, s34
	ds_read_b128 v[160:163], v177 offset:49152
	ds_read_b128 v[164:167], v177 offset:51200
	ds_read_b128 v[216:219], v178 offset:49152
	ds_read_b128 v[220:223], v178 offset:51200
	ds_read_b128 v[224:227], v177 offset:53248
	ds_read_b128 v[228:231], v177 offset:55296
	ds_read_b128 v[232:235], v178 offset:53248
	ds_read_b128 v[236:239], v178 offset:55296
	global_load_lds_dwordx4 v[240:241], off
	s_add_i32 m0, s34, 0x2000
	s_add_u32 s30, s30, 0x80080
	v_lshl_add_u64 v[240:241], v[250:251], 0, s[8:9]
	s_addc_u32 s31, s31, 0
	s_add_i32 s34, s67, s33
	global_load_lds_dwordx4 v[240:241], off
	v_lshl_add_u64 v[240:241], s[30:31], 0, v[146:147]
	s_mov_b32 m0, s34
	s_nop 0
	global_load_lds_dwordx4 v[240:241], off
	v_lshl_add_u64 v[240:241], s[30:31], 0, v[148:149]
	s_add_i32 m0, s34, 0x2000
	s_nop 0
	global_load_lds_dwordx4 v[240:241], off
	s_waitcnt vmcnt(6)
	s_waitcnt lgkmcnt(0)
	s_barrier
	s_setprio 1
	s_waitcnt lgkmcnt(0)
	v_mfma_f32_16x16x32_bf16 v[62:65], v[184:187], v[160:163], v[62:65]
	v_mfma_f32_16x16x32_bf16 v[58:61], v[192:195], v[160:163], v[58:61]
	v_mfma_f32_16x16x32_bf16 v[50:53], v[184:187], v[164:167], v[50:53]
	v_mfma_f32_16x16x32_bf16 v[42:45], v[192:195], v[164:167], v[42:45]
	v_mfma_f32_16x16x32_bf16 v[34:37], v[184:187], v[224:227], v[34:37]
	v_mfma_f32_16x16x32_bf16 v[26:29], v[192:195], v[224:227], v[26:29]
	v_mfma_f32_16x16x32_bf16 v[18:21], v[184:187], v[228:231], v[18:21]
	v_mfma_f32_16x16x32_bf16 v[10:13], v[192:195], v[228:231], v[10:13]
	v_mfma_f32_16x16x32_bf16 v[62:65], v[188:191], v[216:219], v[62:65]
	v_mfma_f32_16x16x32_bf16 v[58:61], v[196:199], v[216:219], v[58:61]
	v_mfma_f32_16x16x32_bf16 v[50:53], v[188:191], v[220:223], v[50:53]
	v_mfma_f32_16x16x32_bf16 v[42:45], v[196:199], v[220:223], v[42:45]
	v_mfma_f32_16x16x32_bf16 v[34:37], v[188:191], v[232:235], v[34:37]
	v_mfma_f32_16x16x32_bf16 v[26:29], v[196:199], v[232:235], v[26:29]
	v_mfma_f32_16x16x32_bf16 v[18:21], v[188:191], v[236:239], v[18:21]
	v_mfma_f32_16x16x32_bf16 v[10:13], v[196:199], v[236:239], v[10:13]
	s_setprio 0
	s_setprio 1
	v_mfma_f32_16x16x32_bf16 v[54:57], v[200:203], v[160:163], v[54:57]
	v_mfma_f32_16x16x32_bf16 v[46:49], v[208:211], v[160:163], v[46:49]
	v_mfma_f32_16x16x32_bf16 v[38:41], v[200:203], v[164:167], v[38:41]
	v_mfma_f32_16x16x32_bf16 v[30:33], v[208:211], v[164:167], v[30:33]
	v_mfma_f32_16x16x32_bf16 v[22:25], v[200:203], v[224:227], v[22:25]
	v_mfma_f32_16x16x32_bf16 v[14:17], v[208:211], v[224:227], v[14:17]
	v_mfma_f32_16x16x32_bf16 v[6:9], v[200:203], v[228:231], v[6:9]
	v_mfma_f32_16x16x32_bf16 v[2:5], v[208:211], v[228:231], v[2:5]
	v_mfma_f32_16x16x32_bf16 v[54:57], v[204:207], v[216:219], v[54:57]
	v_mfma_f32_16x16x32_bf16 v[46:49], v[212:215], v[216:219], v[46:49]
	v_mfma_f32_16x16x32_bf16 v[38:41], v[204:207], v[220:223], v[38:41]
	v_mfma_f32_16x16x32_bf16 v[30:33], v[212:215], v[220:223], v[30:33]
	v_mfma_f32_16x16x32_bf16 v[22:25], v[204:207], v[232:235], v[22:25]
	v_mfma_f32_16x16x32_bf16 v[14:17], v[212:215], v[232:235], v[14:17]
	v_mfma_f32_16x16x32_bf16 v[6:9], v[204:207], v[236:239], v[6:9]
	v_mfma_f32_16x16x32_bf16 v[2:5], v[212:215], v[236:239], v[2:5]
	s_setprio 0
	s_barrier
	s_add_i32 s76, s76, 2
	s_add_u32 s28, s28, 0x100
	s_addc_u32 s29, s29, 0
	s_cmp_gt_u32 s76, 29
	s_cbranch_scc1 .LBB0_389

.LBB0_769:
	s_lshl_b32 s14, s14, 5
	v_lshrrev_b32_e32 v5, 1, v0
	s_ashr_i32 s67, s94, 31
	s_ashr_i32 s1, s0, 31
	s_and_b32 s18, s14, 0x60
	v_and_b32_e32 v3, 15, v0
	v_and_b32_e32 v2, 3, v2
	v_and_b32_e32 v4, 2, v0
	v_and_b32_e32 v5, 4, v5
	s_add_u32 s14, s2, 0x3e800000
	v_bitop3_b32 v4, v5, v2, v4 bitop3:0x36
	v_lshl_or_b32 v207, s15, 6, v3
	s_addc_u32 s15, s3, 0
	v_lshlrev_b32_e32 v4, 4, v4
	v_lshlrev_b32_e32 v5, 7, v207
	v_or_b32_e32 v3, s18, v3
	s_cmpk_lt_u32 s16, 0x100
	v_or_b32_e32 v6, v5, v4
	v_lshlrev_b32_e32 v3, 7, v3
	v_bitop3_b32 v5, v5, 64, v4 bitop3:0x36
	s_cselect_b64 s[16:17], -1, 0
	v_lshl_or_b32 v210, v2, 3, s18
	s_add_u32 s18, s2, 0x56800080
	v_or_b32_e32 v208, v3, v4
	v_bitop3_b32 v209, v3, 64, v4 bitop3:0x36
	v_add_u32_e32 v208, 0x10000, v208
	v_add_u32_e32 v209, 0x10000, v209
	s_addc_u32 s19, s3, 0
	v_mov_b64_e32 v[168:169], s[0:1]
	s_add_i32 s68, 0, 0x10000
	s_add_i32 s69, 0, 0x10800
	s_add_i32 s70, 0, 0x14000
	s_add_i32 s71, 0, 0x14800
	v_add_u32_e32 v211, 0, v6
	v_add_u32_e32 v212, 0, v5
	s_add_i32 s72, 0, 0x18000
	s_add_i32 s73, 0, 0x18800
	s_add_i32 s74, 0, 0x1c000
	s_add_i32 s75, 0, 0x1c800
	s_mov_b32 s20, 0x41000000
	s_mov_b32 s22, 0x39000000
	s_mov_b32 s24, 0x37800000
	s_mov_b32 s76, 0xc0c00000
	s_mov_b32 s77, 0x40000
	s_mov_b32 s78, 0x48000
	s_mov_b32 s79, 0x50000
	v_mov_b32_e32 v213, 0x41000000
	s_branch .LBB0_772
.Lp6_first:
	s_add_u32 s44, s2, s40
	s_addc_u32 s45, s3, s41
	ds_read_b128 v[18:21], v208
	ds_read_b128 v[22:25], v209
	s_add_u32 s84, s44, 0x56800100
	ds_read_b128 v[26:29], v208 offset:2048
	ds_read_b128 v[30:33], v209 offset:2048
	s_addc_u32 s85, s45, 0
	ds_read_b128 v[2:5], v208 offset:16384
	ds_read_b128 v[6:9], v209 offset:16384
	ds_read_b128 v[10:13], v208 offset:18432
	ds_read_b128 v[14:17], v209 offset:18432
	s_and_b64 s[44:45], s[42:43], exec
	s_cselect_b32 s45, s9, s85
	s_cselect_b32 s44, s8, s84
	s_add_u32 s84, s29, s40
	s_addc_u32 s85, s37, s41
	s_and_b64 s[42:43], s[42:43], exec
	s_cselect_b32 s43, s31, s85
	s_cselect_b32 s42, s30, s84
	v_lshl_add_u64 v[200:201], v[190:191], 0, s[40:41]
	s_add_i32 m0, s35, 0x8000
	ds_read_b128 v[218:221], v211
	ds_read_b128 v[226:229], v211 offset:2048
	ds_read_b128 v[222:225], v212
	ds_read_b128 v[230:233], v212 offset:2048
	ds_read_b128 v[234:237], v211 offset:4096
	ds_read_b128 v[242:245], v211 offset:6144
	ds_read_b128 v[238:241], v212 offset:4096
	ds_read_b128 v[246:249], v212 offset:6144
	global_load_lds_dwordx4 v[200:201], off
	v_lshl_add_u64 v[200:201], v[188:189], 0, s[40:41]
	s_add_i32 m0, s35, 0xa000
	s_nop 0
	global_load_lds_dwordx4 v[200:201], off
	v_lshl_add_u64 v[200:201], v[186:187], 0, s[40:41]
	s_add_i32 m0, s35, 0xc000
	s_nop 0
	global_load_lds_dwordx4 v[200:201], off
	v_lshl_add_u64 v[200:201], v[184:185], 0, s[40:41]
	s_add_i32 m0, s35, 0xe000
	s_nop 0
	global_load_lds_dwordx4 v[200:201], off
	s_waitcnt vmcnt(8)
	s_waitcnt lgkmcnt(0)
	s_barrier
	s_setprio 1
	s_waitcnt lgkmcnt(0)
	v_mfma_f32_16x16x128_f8f6f4 v[158:161], v[18:25], v[218:225], 0
	v_mfma_f32_16x16x128_f8f6f4 v[154:157], v[26:33], v[218:225], 0
	v_mfma_f32_16x16x128_f8f6f4 v[150:153], v[18:25], v[226:233], 0
	v_mfma_f32_16x16x128_f8f6f4 v[146:149], v[26:33], v[226:233], 0
	v_mfma_f32_16x16x128_f8f6f4 v[126:129], v[18:25], v[234:241], 0
	v_mfma_f32_16x16x128_f8f6f4 v[122:125], v[26:33], v[234:241], 0
	v_mfma_f32_16x16x128_f8f6f4 v[110:113], v[18:25], v[242:249], 0
	v_mfma_f32_16x16x128_f8f6f4 v[106:109], v[26:33], v[242:249], 0
	s_setprio 0
	s_setprio 1
	v_mfma_f32_16x16x128_f8f6f4 v[142:145], v[2:9], v[218:225], 0
	v_mfma_f32_16x16x128_f8f6f4 v[138:141], v[10:17], v[218:225], 0
	v_mfma_f32_16x16x128_f8f6f4 v[134:137], v[2:9], v[226:233], 0
	v_mfma_f32_16x16x128_f8f6f4 v[130:133], v[10:17], v[226:233], 0
	v_mfma_f32_16x16x128_f8f6f4 v[118:121], v[2:9], v[234:241], 0
	v_mfma_f32_16x16x128_f8f6f4 v[114:117], v[10:17], v[234:241], 0
	v_mfma_f32_16x16x128_f8f6f4 v[102:105], v[2:9], v[242:249], 0
	v_mfma_f32_16x16x128_f8f6f4 v[98:101], v[10:17], v[242:249], 0
	s_setprio 0
	s_barrier
	s_add_i32 s84, s68, s33
	v_lshl_add_u64 v[200:201], s[42:43], 0, v[164:165]
	s_mov_b32 m0, s84
	ds_read_b128 v[218:221], v211 offset:16384
	ds_read_b128 v[226:229], v211 offset:18432
	ds_read_b128 v[222:225], v212 offset:16384
	ds_read_b128 v[230:233], v212 offset:18432
	ds_read_b128 v[234:237], v211 offset:20480
	ds_read_b128 v[242:245], v211 offset:22528
	ds_read_b128 v[238:241], v212 offset:20480
	ds_read_b128 v[246:249], v212 offset:22528
	global_load_lds_dwordx4 v[200:201], off
	s_add_i32 m0, s84, 0x2000
	s_add_u32 s84, s42, 0x40000
	v_lshl_add_u64 v[202:203], s[42:43], 0, v[166:167]
	s_addc_u32 s85, s43, 0
	s_add_i32 s86, s70, s33
	global_load_lds_dwordx4 v[202:203], off
	v_lshl_add_u64 v[250:251], s[84:85], 0, v[164:165]
	s_mov_b32 m0, s86
	s_nop 0
	global_load_lds_dwordx4 v[250:251], off
	v_lshl_add_u64 v[250:251], s[84:85], 0, v[166:167]
	s_add_i32 m0, s86, 0x2000
	s_nop 0
	global_load_lds_dwordx4 v[250:251], off
	s_waitcnt vmcnt(6)
	s_waitcnt lgkmcnt(0)
	s_barrier
	s_setprio 1
	s_waitcnt lgkmcnt(0)
	v_mfma_f32_16x16x128_f8f6f4 v[94:97], v[18:25], v[218:225], 0
	v_mfma_f32_16x16x128_f8f6f4 v[90:93], v[26:33], v[218:225], 0
	v_mfma_f32_16x16x128_f8f6f4 v[78:81], v[18:25], v[226:233], 0
	v_mfma_f32_16x16x128_f8f6f4 v[74:77], v[26:33], v[226:233], 0
	v_mfma_f32_16x16x128_f8f6f4 v[62:65], v[18:25], v[234:241], 0
	v_mfma_f32_16x16x128_f8f6f4 v[58:61], v[26:33], v[234:241], 0
	v_mfma_f32_16x16x128_f8f6f4 v[46:49], v[18:25], v[242:249], 0
	v_mfma_f32_16x16x128_f8f6f4 v[42:45], v[26:33], v[242:249], 0
	s_setprio 0
	s_setprio 1
	v_mfma_f32_16x16x128_f8f6f4 v[86:89], v[2:9], v[218:225], 0
	v_mfma_f32_16x16x128_f8f6f4 v[82:85], v[10:17], v[218:225], 0
	v_mfma_f32_16x16x128_f8f6f4 v[70:73], v[2:9], v[226:233], 0
	v_mfma_f32_16x16x128_f8f6f4 v[66:69], v[10:17], v[226:233], 0
	v_mfma_f32_16x16x128_f8f6f4 v[54:57], v[2:9], v[234:241], 0
	v_mfma_f32_16x16x128_f8f6f4 v[50:53], v[10:17], v[234:241], 0
	v_mfma_f32_16x16x128_f8f6f4 v[38:41], v[2:9], v[242:249], 0
	v_mfma_f32_16x16x128_f8f6f4 v[34:37], v[10:17], v[242:249], 0
	s_setprio 0
	s_barrier
	s_branch .Lp6_blk3

.LBB0_777:
	s_cmp_eq_u32 s40, 0
	s_cbranch_scc1 .Lp6_first
	s_add_u32 s44, s2, s40
	s_addc_u32 s45, s3, s41
	ds_read_b128 v[18:21], v208
	ds_read_b128 v[22:25], v209
	s_add_u32 s84, s44, 0x56800100
	ds_read_b128 v[26:29], v208 offset:2048
	ds_read_b128 v[30:33], v209 offset:2048
	s_addc_u32 s85, s45, 0
	ds_read_b128 v[2:5], v208 offset:16384
	ds_read_b128 v[6:9], v209 offset:16384
	ds_read_b128 v[10:13], v208 offset:18432
	ds_read_b128 v[14:17], v209 offset:18432
	s_and_b64 s[44:45], s[42:43], exec
	s_cselect_b32 s45, s9, s85
	s_cselect_b32 s44, s8, s84
	s_add_u32 s84, s29, s40
	s_addc_u32 s85, s37, s41
	s_and_b64 s[42:43], s[42:43], exec
	s_cselect_b32 s43, s31, s85
	s_cselect_b32 s42, s30, s84
	v_lshl_add_u64 v[200:201], v[190:191], 0, s[40:41]
	s_add_i32 m0, s35, 0x8000
	ds_read_b128 v[218:221], v211
	ds_read_b128 v[226:229], v211 offset:2048
	ds_read_b128 v[222:225], v212
	ds_read_b128 v[230:233], v212 offset:2048
	ds_read_b128 v[234:237], v211 offset:4096
	ds_read_b128 v[242:245], v211 offset:6144
	ds_read_b128 v[238:241], v212 offset:4096
	ds_read_b128 v[246:249], v212 offset:6144
	global_load_lds_dwordx4 v[200:201], off
	v_lshl_add_u64 v[200:201], v[188:189], 0, s[40:41]
	s_add_i32 m0, s35, 0xa000
	s_nop 0
	global_load_lds_dwordx4 v[200:201], off
	v_lshl_add_u64 v[200:201], v[186:187], 0, s[40:41]
	s_add_i32 m0, s35, 0xc000
	s_nop 0
	global_load_lds_dwordx4 v[200:201], off
	v_lshl_add_u64 v[200:201], v[184:185], 0, s[40:41]
	s_add_i32 m0, s35, 0xe000
	s_nop 0
	global_load_lds_dwordx4 v[200:201], off
	s_waitcnt vmcnt(8)
	s_waitcnt lgkmcnt(0)
	s_barrier
	s_setprio 1
	s_waitcnt lgkmcnt(0)
	v_mfma_f32_16x16x128_f8f6f4 v[158:161], v[18:25], v[218:225], v[158:161]
	v_mfma_f32_16x16x128_f8f6f4 v[154:157], v[26:33], v[218:225], v[154:157]
	v_mfma_f32_16x16x128_f8f6f4 v[150:153], v[18:25], v[226:233], v[150:153]
	v_mfma_f32_16x16x128_f8f6f4 v[146:149], v[26:33], v[226:233], v[146:149]
	v_mfma_f32_16x16x128_f8f6f4 v[126:129], v[18:25], v[234:241], v[126:129]
	v_mfma_f32_16x16x128_f8f6f4 v[122:125], v[26:33], v[234:241], v[122:125]
	v_mfma_f32_16x16x128_f8f6f4 v[110:113], v[18:25], v[242:249], v[110:113]
	v_mfma_f32_16x16x128_f8f6f4 v[106:109], v[26:33], v[242:249], v[106:109]
	s_setprio 0
	s_setprio 1
	v_mfma_f32_16x16x128_f8f6f4 v[142:145], v[2:9], v[218:225], v[142:145]
	v_mfma_f32_16x16x128_f8f6f4 v[138:141], v[10:17], v[218:225], v[138:141]
	v_mfma_f32_16x16x128_f8f6f4 v[134:137], v[2:9], v[226:233], v[134:137]
	v_mfma_f32_16x16x128_f8f6f4 v[130:133], v[10:17], v[226:233], v[130:133]
	v_mfma_f32_16x16x128_f8f6f4 v[118:121], v[2:9], v[234:241], v[118:121]
	v_mfma_f32_16x16x128_f8f6f4 v[114:117], v[10:17], v[234:241], v[114:117]
	v_mfma_f32_16x16x128_f8f6f4 v[102:105], v[2:9], v[242:249], v[102:105]
	v_mfma_f32_16x16x128_f8f6f4 v[98:101], v[10:17], v[242:249], v[98:101]
	s_setprio 0
	s_barrier
	s_add_i32 s84, s68, s33
	v_lshl_add_u64 v[200:201], s[42:43], 0, v[164:165]
	s_mov_b32 m0, s84
	ds_read_b128 v[218:221], v211 offset:16384
	ds_read_b128 v[226:229], v211 offset:18432
	ds_read_b128 v[222:225], v212 offset:16384
	ds_read_b128 v[230:233], v212 offset:18432
	ds_read_b128 v[234:237], v211 offset:20480
	ds_read_b128 v[242:245], v211 offset:22528
	ds_read_b128 v[238:241], v212 offset:20480
	ds_read_b128 v[246:249], v212 offset:22528
	global_load_lds_dwordx4 v[200:201], off
	s_add_i32 m0, s84, 0x2000
	s_add_u32 s84, s42, 0x40000
	v_lshl_add_u64 v[202:203], s[42:43], 0, v[166:167]
	s_addc_u32 s85, s43, 0
	s_add_i32 s86, s70, s33
	global_load_lds_dwordx4 v[202:203], off
	v_lshl_add_u64 v[250:251], s[84:85], 0, v[164:165]
	s_mov_b32 m0, s86
	s_nop 0
	global_load_lds_dwordx4 v[250:251], off
	v_lshl_add_u64 v[250:251], s[84:85], 0, v[166:167]
	s_add_i32 m0, s86, 0x2000
	s_nop 0
	global_load_lds_dwordx4 v[250:251], off
	s_waitcnt vmcnt(6)
	s_waitcnt lgkmcnt(0)
	s_barrier
	s_setprio 1
	s_waitcnt lgkmcnt(0)
	v_mfma_f32_16x16x128_f8f6f4 v[94:97], v[18:25], v[218:225], v[94:97]
	v_mfma_f32_16x16x128_f8f6f4 v[90:93], v[26:33], v[218:225], v[90:93]
	v_mfma_f32_16x16x128_f8f6f4 v[78:81], v[18:25], v[226:233], v[78:81]
	v_mfma_f32_16x16x128_f8f6f4 v[74:77], v[26:33], v[226:233], v[74:77]
	v_mfma_f32_16x16x128_f8f6f4 v[62:65], v[18:25], v[234:241], v[62:65]
	v_mfma_f32_16x16x128_f8f6f4 v[58:61], v[26:33], v[234:241], v[58:61]
	v_mfma_f32_16x16x128_f8f6f4 v[46:49], v[18:25], v[242:249], v[46:49]
	v_mfma_f32_16x16x128_f8f6f4 v[42:45], v[26:33], v[242:249], v[42:45]
	s_setprio 0
	s_setprio 1
	v_mfma_f32_16x16x128_f8f6f4 v[86:89], v[2:9], v[218:225], v[86:89]
	v_mfma_f32_16x16x128_f8f6f4 v[82:85], v[10:17], v[218:225], v[82:85]
	v_mfma_f32_16x16x128_f8f6f4 v[70:73], v[2:9], v[226:233], v[70:73]
	v_mfma_f32_16x16x128_f8f6f4 v[66:69], v[10:17], v[226:233], v[66:69]
	v_mfma_f32_16x16x128_f8f6f4 v[54:57], v[2:9], v[234:241], v[54:57]
	v_mfma_f32_16x16x128_f8f6f4 v[50:53], v[10:17], v[234:241], v[50:53]
	v_mfma_f32_16x16x128_f8f6f4 v[38:41], v[2:9], v[242:249], v[38:41]
	v_mfma_f32_16x16x128_f8f6f4 v[34:37], v[10:17], v[242:249], v[34:37]
	s_setprio 0
	s_barrier
.Lp6_blk3:
	ds_read_b128 v[2:5], v208 offset:32768
	ds_read_b128 v[6:9], v209 offset:32768
	ds_read_b128 v[10:13], v208 offset:34816
	ds_read_b128 v[14:17], v209 offset:34816
	ds_read_b128 v[18:21], v208 offset:49152
	ds_read_b128 v[22:25], v209 offset:49152
	ds_read_b128 v[26:29], v208 offset:51200
	ds_read_b128 v[30:33], v209 offset:51200
	s_mov_b32 m0, s35
	v_lshl_add_u64 v[198:199], s[44:45], 0, v[198:199]
	ds_read_b128 v[218:221], v211 offset:32768
	ds_read_b128 v[226:229], v211 offset:34816
	ds_read_b128 v[222:225], v212 offset:32768
	ds_read_b128 v[230:233], v212 offset:34816
	ds_read_b128 v[234:237], v211 offset:36864
	ds_read_b128 v[242:245], v211 offset:38912
	ds_read_b128 v[238:241], v212 offset:36864
	ds_read_b128 v[246:249], v212 offset:38912
	global_load_lds_dwordx4 v[198:199], off
	v_lshl_add_u64 v[196:197], s[44:45], 0, v[196:197]
	s_mov_b32 m0, s55
	v_lshl_add_u64 v[194:195], s[44:45], 0, v[194:195]
	global_load_lds_dwordx4 v[196:197], off
	s_mov_b32 m0, s64
	v_lshl_add_u64 v[192:193], s[44:45], 0, v[192:193]
	global_load_lds_dwordx4 v[194:195], off
	s_mov_b32 m0, s65
	s_nop 0
	global_load_lds_dwordx4 v[192:193], off
	s_waitcnt vmcnt(8)
	s_waitcnt lgkmcnt(0)
	s_barrier
	s_setprio 1
	s_waitcnt lgkmcnt(0)
	v_mfma_f32_16x16x128_f8f6f4 v[158:161], v[2:9], v[218:225], v[158:161]
	v_mfma_f32_16x16x128_f8f6f4 v[154:157], v[10:17], v[218:225], v[154:157]
	v_mfma_f32_16x16x128_f8f6f4 v[150:153], v[2:9], v[226:233], v[150:153]
	v_mfma_f32_16x16x128_f8f6f4 v[146:149], v[10:17], v[226:233], v[146:149]
	v_mfma_f32_16x16x128_f8f6f4 v[126:129], v[2:9], v[234:241], v[126:129]
	v_mfma_f32_16x16x128_f8f6f4 v[122:125], v[10:17], v[234:241], v[122:125]
	v_mfma_f32_16x16x128_f8f6f4 v[110:113], v[2:9], v[242:249], v[110:113]
	v_mfma_f32_16x16x128_f8f6f4 v[106:109], v[10:17], v[242:249], v[106:109]
	s_setprio 0
	s_setprio 1
	v_mfma_f32_16x16x128_f8f6f4 v[142:145], v[18:25], v[218:225], v[142:145]
	v_mfma_f32_16x16x128_f8f6f4 v[138:141], v[26:33], v[218:225], v[138:141]
	v_mfma_f32_16x16x128_f8f6f4 v[134:137], v[18:25], v[226:233], v[134:137]
	v_mfma_f32_16x16x128_f8f6f4 v[130:133], v[26:33], v[226:233], v[130:133]
	v_mfma_f32_16x16x128_f8f6f4 v[118:121], v[18:25], v[234:241], v[118:121]
	v_mfma_f32_16x16x128_f8f6f4 v[114:117], v[26:33], v[234:241], v[114:117]
	v_mfma_f32_16x16x128_f8f6f4 v[102:105], v[18:25], v[242:249], v[102:105]
	v_mfma_f32_16x16x128_f8f6f4 v[98:101], v[26:33], v[242:249], v[98:101]
	s_setprio 0
	s_barrier
	s_add_i32 s44, s72, s33
	v_lshl_add_u64 v[200:201], v[200:201], 0, s[10:11]
	s_mov_b32 m0, s44
	ds_read_b128 v[192:195], v211 offset:49152
	ds_read_b128 v[218:221], v211 offset:51200
	ds_read_b128 v[196:199], v212 offset:49152
	ds_read_b128 v[222:225], v212 offset:51200
	ds_read_b128 v[226:229], v211 offset:53248
	ds_read_b128 v[234:237], v211 offset:55296
	ds_read_b128 v[230:233], v212 offset:53248
	ds_read_b128 v[238:241], v212 offset:55296
	global_load_lds_dwordx4 v[200:201], off
	s_add_i32 m0, s44, 0x2000
	s_add_u32 s42, s42, 0x40080
	v_lshl_add_u64 v[200:201], v[202:203], 0, s[10:11]
	s_addc_u32 s43, s43, 0
	s_add_i32 s44, s74, s33
	global_load_lds_dwordx4 v[200:201], off
	v_lshl_add_u64 v[200:201], s[42:43], 0, v[164:165]
	s_mov_b32 m0, s44
	s_nop 0
	global_load_lds_dwordx4 v[200:201], off
	v_lshl_add_u64 v[200:201], s[42:43], 0, v[166:167]
	s_add_i32 m0, s44, 0x2000
	s_nop 0
	global_load_lds_dwordx4 v[200:201], off
	s_waitcnt vmcnt(6)
	s_waitcnt lgkmcnt(0)
	s_barrier
	s_setprio 1
	s_waitcnt lgkmcnt(0)
	v_mfma_f32_16x16x128_f8f6f4 v[94:97], v[2:9], v[192:199], v[94:97]
	v_mfma_f32_16x16x128_f8f6f4 v[90:93], v[10:17], v[192:199], v[90:93]
	v_mfma_f32_16x16x128_f8f6f4 v[78:81], v[2:9], v[218:225], v[78:81]
	v_mfma_f32_16x16x128_f8f6f4 v[74:77], v[10:17], v[218:225], v[74:77]
	v_mfma_f32_16x16x128_f8f6f4 v[62:65], v[2:9], v[226:233], v[62:65]
	v_mfma_f32_16x16x128_f8f6f4 v[58:61], v[10:17], v[226:233], v[58:61]
	v_mfma_f32_16x16x128_f8f6f4 v[46:49], v[2:9], v[234:241], v[46:49]
	v_mfma_f32_16x16x128_f8f6f4 v[42:45], v[10:17], v[234:241], v[42:45]
	s_setprio 0
	s_setprio 1
	v_mfma_f32_16x16x128_f8f6f4 v[86:89], v[18:25], v[192:199], v[86:89]
	v_mfma_f32_16x16x128_f8f6f4 v[82:85], v[26:33], v[192:199], v[82:85]
	v_mfma_f32_16x16x128_f8f6f4 v[70:73], v[18:25], v[218:225], v[70:73]
	v_mfma_f32_16x16x128_f8f6f4 v[66:69], v[26:33], v[218:225], v[66:69]
	v_mfma_f32_16x16x128_f8f6f4 v[54:57], v[18:25], v[226:233], v[54:57]
	v_mfma_f32_16x16x128_f8f6f4 v[50:53], v[26:33], v[226:233], v[50:53]
	v_mfma_f32_16x16x128_f8f6f4 v[38:41], v[18:25], v[234:241], v[38:41]
	v_mfma_f32_16x16x128_f8f6f4 v[34:37], v[26:33], v[234:241], v[34:37]
	s_setprio 0
	s_barrier
	s_add_i32 s83, s83, 2
	s_add_u32 s40, s40, 0x100
	s_addc_u32 s41, s41, 0
	s_cmp_gt_u32 s83, 13
	s_cbranch_scc1 .LBB0_781

.LBB0_856:
	s_add_u32 s16, s2, 0x50800000
	v_lshrrev_b32_e32 v5, 1, v0
	s_addc_u32 s17, s3, 0
	v_and_b32_e32 v3, 15, v0
	v_and_b32_e32 v2, 3, v2
	v_and_b32_e32 v4, 2, v0
	v_and_b32_e32 v5, 4, v5
	s_lshl_b32 s19, s19, 5
	v_bitop3_b32 v4, v5, v2, v4 bitop3:0x36
	s_ashr_i32 s65, s94, 31
	s_ashr_i32 s1, s0, 31
	v_lshl_or_b32 v209, s20, 6, v3
	s_and_b32 s20, s19, 0x60
	v_lshlrev_b32_e32 v4, 4, v4
	v_lshlrev_b32_e32 v5, 7, v209
	v_or_b32_e32 v3, s20, v3
	s_cmpk_lt_u32 s18, 0x100
	v_or_b32_e32 v6, v5, v4
	v_lshlrev_b32_e32 v3, 7, v3
	v_bitop3_b32 v5, v5, 64, v4 bitop3:0x36
	s_cselect_b64 s[18:19], -1, 0
	v_lshl_or_b32 v212, v2, 3, s20
	s_add_u32 s20, s2, 0x3e800080
	v_or_b32_e32 v210, v3, v4
	v_bitop3_b32 v211, v3, 64, v4 bitop3:0x36
	v_add_u32_e32 v210, 0x10000, v210
	v_add_u32_e32 v211, 0x10000, v211
	s_addc_u32 s21, s3, 0
	v_mov_b64_e32 v[168:169], s[0:1]
	s_add_i32 s66, 0, 0x10000
	s_add_i32 s67, 0, 0x10800
	s_add_i32 s68, 0, 0x14000
	s_add_i32 s69, 0, 0x14800
	v_add_u32_e32 v213, 0, v6
	v_add_u32_e32 v214, 0, v5
	s_add_i32 s70, 0, 0x18000
	s_add_i32 s71, 0, 0x18800
	s_add_i32 s72, 0, 0x1c000
	s_add_i32 s73, 0, 0x1c800
	s_mov_b32 s22, 0x42800000
	s_mov_b32 s24, 0x3b000000
	s_mov_b32 s74, 0xc3e00000
	s_mov_b32 s75, 0x40000
	s_mov_b64 s[26:27], 0x48000
	s_mov_b32 s76, 0x48000
	s_mov_b64 s[28:29], 0x50000
	s_mov_b32 s77, 0x50000
	s_mov_b64 s[30:31], 0x58000
	s_mov_b32 s78, 0x58000
	v_mov_b32_e32 v215, 0x43e00000
	s_mov_b64 s[38:39], s[44:45]
	s_branch .LBB0_859
.Lp7_first:
	s_add_u32 s48, s2, s44
	s_addc_u32 s49, s3, s45
	ds_read_b128 v[18:21], v210
	ds_read_b128 v[22:25], v211
	s_add_u32 s81, s48, 0x3e800100
	ds_read_b128 v[26:29], v210 offset:2048
	ds_read_b128 v[30:33], v211 offset:2048
	s_addc_u32 s82, s49, 0
	ds_read_b128 v[2:5], v210 offset:16384
	ds_read_b128 v[6:9], v211 offset:16384
	ds_read_b128 v[10:13], v210 offset:18432
	ds_read_b128 v[14:17], v211 offset:18432
	s_and_b64 s[48:49], s[46:47], exec
	s_cselect_b32 s49, s9, s82
	s_cselect_b32 s48, s8, s81
	s_add_u32 s81, s35, s44
	s_addc_u32 s82, s37, s45
	s_and_b64 s[46:47], s[46:47], exec
	s_cselect_b32 s47, s39, s82
	s_cselect_b32 s46, s38, s81
	v_lshl_add_u64 v[200:201], v[190:191], 0, s[44:45]
	s_add_i32 m0, s41, 0x8000
	ds_read_b128 v[220:223], v213
	ds_read_b128 v[228:231], v213 offset:2048
	ds_read_b128 v[224:227], v214
	ds_read_b128 v[232:235], v214 offset:2048
	ds_read_b128 v[236:239], v213 offset:4096
	ds_read_b128 v[244:247], v213 offset:6144
	ds_read_b128 v[240:243], v214 offset:4096
	ds_read_b128 v[248:251], v214 offset:6144
	global_load_lds_dwordx4 v[200:201], off
	v_lshl_add_u64 v[200:201], v[188:189], 0, s[44:45]
	s_add_i32 m0, s41, 0xa000
	s_nop 0
	global_load_lds_dwordx4 v[200:201], off
	v_lshl_add_u64 v[200:201], v[186:187], 0, s[44:45]
	s_add_i32 m0, s41, 0xc000
	s_nop 0
	global_load_lds_dwordx4 v[200:201], off
	v_lshl_add_u64 v[200:201], v[184:185], 0, s[44:45]
	s_add_i32 m0, s41, 0xe000
	s_nop 0
	global_load_lds_dwordx4 v[200:201], off
	s_waitcnt vmcnt(8)
	s_waitcnt lgkmcnt(0)
	s_barrier
	s_setprio 1
	s_waitcnt lgkmcnt(0)
	v_mfma_f32_16x16x128_f8f6f4 v[158:161], v[18:25], v[220:227], 0
	v_mfma_f32_16x16x128_f8f6f4 v[154:157], v[26:33], v[220:227], 0
	v_mfma_f32_16x16x128_f8f6f4 v[150:153], v[18:25], v[228:235], 0
	v_mfma_f32_16x16x128_f8f6f4 v[146:149], v[26:33], v[228:235], 0
	v_mfma_f32_16x16x128_f8f6f4 v[142:145], v[18:25], v[236:243], 0
	v_mfma_f32_16x16x128_f8f6f4 v[138:141], v[26:33], v[236:243], 0
	v_mfma_f32_16x16x128_f8f6f4 v[134:137], v[18:25], v[244:251], 0
	v_mfma_f32_16x16x128_f8f6f4 v[130:133], v[26:33], v[244:251], 0
	s_setprio 0
	s_setprio 1
	v_mfma_f32_16x16x128_f8f6f4 v[102:105], v[2:9], v[220:227], 0
	v_mfma_f32_16x16x128_f8f6f4 v[94:97], v[10:17], v[220:227], 0
	v_mfma_f32_16x16x128_f8f6f4 v[86:89], v[2:9], v[228:235], 0
	v_mfma_f32_16x16x128_f8f6f4 v[82:85], v[10:17], v[228:235], 0
	v_mfma_f32_16x16x128_f8f6f4 v[78:81], v[2:9], v[236:243], 0
	v_mfma_f32_16x16x128_f8f6f4 v[74:77], v[10:17], v[236:243], 0
	v_mfma_f32_16x16x128_f8f6f4 v[70:73], v[2:9], v[244:251], 0
	v_mfma_f32_16x16x128_f8f6f4 v[66:69], v[10:17], v[244:251], 0
	s_setprio 0
	s_barrier
	s_add_i32 s81, s66, s51
	v_lshl_add_u64 v[200:201], s[46:47], 0, v[162:163]
	s_mov_b32 m0, s81
	ds_read_b128 v[220:223], v213 offset:16384
	ds_read_b128 v[228:231], v213 offset:18432
	ds_read_b128 v[224:227], v214 offset:16384
	ds_read_b128 v[232:235], v214 offset:18432
	ds_read_b128 v[236:239], v213 offset:20480
	ds_read_b128 v[244:247], v213 offset:22528
	ds_read_b128 v[240:243], v214 offset:20480
	ds_read_b128 v[248:251], v214 offset:22528
	global_load_lds_dwordx4 v[200:201], off
	s_add_i32 m0, s81, 0x2000
	s_add_u32 s82, s46, 0x40000
	v_lshl_add_u64 v[202:203], s[46:47], 0, v[164:165]
	s_addc_u32 s83, s47, 0
	s_add_i32 s81, s68, s51
	global_load_lds_dwordx4 v[202:203], off
	v_lshl_add_u64 v[252:253], s[82:83], 0, v[162:163]
	s_mov_b32 m0, s81
	s_nop 0
	global_load_lds_dwordx4 v[252:253], off
	v_lshl_add_u64 v[252:253], s[82:83], 0, v[164:165]
	s_add_i32 m0, s81, 0x2000
	s_nop 0
	global_load_lds_dwordx4 v[252:253], off
	s_waitcnt vmcnt(6)
	s_waitcnt lgkmcnt(0)
	s_barrier
	s_setprio 1
	s_waitcnt lgkmcnt(0)
	v_mfma_f32_16x16x128_f8f6f4 v[126:129], v[18:25], v[220:227], 0
	v_mfma_f32_16x16x128_f8f6f4 v[122:125], v[26:33], v[220:227], 0
	v_mfma_f32_16x16x128_f8f6f4 v[118:121], v[18:25], v[228:235], 0
	v_mfma_f32_16x16x128_f8f6f4 v[114:117], v[26:33], v[228:235], 0
	v_mfma_f32_16x16x128_f8f6f4 v[110:113], v[18:25], v[236:243], 0
	v_mfma_f32_16x16x128_f8f6f4 v[106:109], v[26:33], v[236:243], 0
	v_mfma_f32_16x16x128_f8f6f4 v[98:101], v[18:25], v[244:251], 0
	v_mfma_f32_16x16x128_f8f6f4 v[90:93], v[26:33], v[244:251], 0
	s_setprio 0
	s_setprio 1
	v_mfma_f32_16x16x128_f8f6f4 v[62:65], v[2:9], v[220:227], 0
	v_mfma_f32_16x16x128_f8f6f4 v[58:61], v[10:17], v[220:227], 0
	v_mfma_f32_16x16x128_f8f6f4 v[54:57], v[2:9], v[228:235], 0
	v_mfma_f32_16x16x128_f8f6f4 v[50:53], v[10:17], v[228:235], 0
	v_mfma_f32_16x16x128_f8f6f4 v[46:49], v[2:9], v[236:243], 0
	v_mfma_f32_16x16x128_f8f6f4 v[42:45], v[10:17], v[236:243], 0
	v_mfma_f32_16x16x128_f8f6f4 v[38:41], v[2:9], v[244:251], 0
	v_mfma_f32_16x16x128_f8f6f4 v[34:37], v[10:17], v[244:251], 0
	s_setprio 0
	s_barrier
	s_branch .Lp7_blk3

.LBB0_862:
	s_cmp_eq_u32 s44, 0
	s_cbranch_scc1 .Lp7_first
	s_add_u32 s48, s2, s44
	s_addc_u32 s49, s3, s45
	ds_read_b128 v[18:21], v210
	ds_read_b128 v[22:25], v211
	s_add_u32 s81, s48, 0x3e800100
	ds_read_b128 v[26:29], v210 offset:2048
	ds_read_b128 v[30:33], v211 offset:2048
	s_addc_u32 s82, s49, 0
	ds_read_b128 v[2:5], v210 offset:16384
	ds_read_b128 v[6:9], v211 offset:16384
	ds_read_b128 v[10:13], v210 offset:18432
	ds_read_b128 v[14:17], v211 offset:18432
	s_and_b64 s[48:49], s[46:47], exec
	s_cselect_b32 s49, s9, s82
	s_cselect_b32 s48, s8, s81
	s_add_u32 s81, s35, s44
	s_addc_u32 s82, s37, s45
	s_and_b64 s[46:47], s[46:47], exec
	s_cselect_b32 s47, s39, s82
	s_cselect_b32 s46, s38, s81
	v_lshl_add_u64 v[200:201], v[190:191], 0, s[44:45]
	s_add_i32 m0, s41, 0x8000
	ds_read_b128 v[220:223], v213
	ds_read_b128 v[228:231], v213 offset:2048
	ds_read_b128 v[224:227], v214
	ds_read_b128 v[232:235], v214 offset:2048
	ds_read_b128 v[236:239], v213 offset:4096
	ds_read_b128 v[244:247], v213 offset:6144
	ds_read_b128 v[240:243], v214 offset:4096
	ds_read_b128 v[248:251], v214 offset:6144
	global_load_lds_dwordx4 v[200:201], off
	v_lshl_add_u64 v[200:201], v[188:189], 0, s[44:45]
	s_add_i32 m0, s41, 0xa000
	s_nop 0
	global_load_lds_dwordx4 v[200:201], off
	v_lshl_add_u64 v[200:201], v[186:187], 0, s[44:45]
	s_add_i32 m0, s41, 0xc000
	s_nop 0
	global_load_lds_dwordx4 v[200:201], off
	v_lshl_add_u64 v[200:201], v[184:185], 0, s[44:45]
	s_add_i32 m0, s41, 0xe000
	s_nop 0
	global_load_lds_dwordx4 v[200:201], off
	s_waitcnt vmcnt(8)
	s_waitcnt lgkmcnt(0)
	s_barrier
	s_setprio 1
	s_waitcnt lgkmcnt(0)
	v_mfma_f32_16x16x128_f8f6f4 v[158:161], v[18:25], v[220:227], v[158:161]
	v_mfma_f32_16x16x128_f8f6f4 v[154:157], v[26:33], v[220:227], v[154:157]
	v_mfma_f32_16x16x128_f8f6f4 v[150:153], v[18:25], v[228:235], v[150:153]
	v_mfma_f32_16x16x128_f8f6f4 v[146:149], v[26:33], v[228:235], v[146:149]
	v_mfma_f32_16x16x128_f8f6f4 v[142:145], v[18:25], v[236:243], v[142:145]
	v_mfma_f32_16x16x128_f8f6f4 v[138:141], v[26:33], v[236:243], v[138:141]
	v_mfma_f32_16x16x128_f8f6f4 v[134:137], v[18:25], v[244:251], v[134:137]
	v_mfma_f32_16x16x128_f8f6f4 v[130:133], v[26:33], v[244:251], v[130:133]
	s_setprio 0
	s_setprio 1
	v_mfma_f32_16x16x128_f8f6f4 v[102:105], v[2:9], v[220:227], v[102:105]
	v_mfma_f32_16x16x128_f8f6f4 v[94:97], v[10:17], v[220:227], v[94:97]
	v_mfma_f32_16x16x128_f8f6f4 v[86:89], v[2:9], v[228:235], v[86:89]
	v_mfma_f32_16x16x128_f8f6f4 v[82:85], v[10:17], v[228:235], v[82:85]
	v_mfma_f32_16x16x128_f8f6f4 v[78:81], v[2:9], v[236:243], v[78:81]
	v_mfma_f32_16x16x128_f8f6f4 v[74:77], v[10:17], v[236:243], v[74:77]
	v_mfma_f32_16x16x128_f8f6f4 v[70:73], v[2:9], v[244:251], v[70:73]
	v_mfma_f32_16x16x128_f8f6f4 v[66:69], v[10:17], v[244:251], v[66:69]
	s_setprio 0
	s_barrier
	s_add_i32 s81, s66, s51
	v_lshl_add_u64 v[200:201], s[46:47], 0, v[162:163]
	s_mov_b32 m0, s81
	ds_read_b128 v[220:223], v213 offset:16384
	ds_read_b128 v[228:231], v213 offset:18432
	ds_read_b128 v[224:227], v214 offset:16384
	ds_read_b128 v[232:235], v214 offset:18432
	ds_read_b128 v[236:239], v213 offset:20480
	ds_read_b128 v[244:247], v213 offset:22528
	ds_read_b128 v[240:243], v214 offset:20480
	ds_read_b128 v[248:251], v214 offset:22528
	global_load_lds_dwordx4 v[200:201], off
	s_add_i32 m0, s81, 0x2000
	s_add_u32 s82, s46, 0x40000
	v_lshl_add_u64 v[202:203], s[46:47], 0, v[164:165]
	s_addc_u32 s83, s47, 0
	s_add_i32 s81, s68, s51
	global_load_lds_dwordx4 v[202:203], off
	v_lshl_add_u64 v[252:253], s[82:83], 0, v[162:163]
	s_mov_b32 m0, s81
	s_nop 0
	global_load_lds_dwordx4 v[252:253], off
	v_lshl_add_u64 v[252:253], s[82:83], 0, v[164:165]
	s_add_i32 m0, s81, 0x2000
	s_nop 0
	global_load_lds_dwordx4 v[252:253], off
	s_waitcnt vmcnt(6)
	s_waitcnt lgkmcnt(0)
	s_barrier
	s_setprio 1
	s_waitcnt lgkmcnt(0)
	v_mfma_f32_16x16x128_f8f6f4 v[126:129], v[18:25], v[220:227], v[126:129]
	v_mfma_f32_16x16x128_f8f6f4 v[122:125], v[26:33], v[220:227], v[122:125]
	v_mfma_f32_16x16x128_f8f6f4 v[118:121], v[18:25], v[228:235], v[118:121]
	v_mfma_f32_16x16x128_f8f6f4 v[114:117], v[26:33], v[228:235], v[114:117]
	v_mfma_f32_16x16x128_f8f6f4 v[110:113], v[18:25], v[236:243], v[110:113]
	v_mfma_f32_16x16x128_f8f6f4 v[106:109], v[26:33], v[236:243], v[106:109]
	v_mfma_f32_16x16x128_f8f6f4 v[98:101], v[18:25], v[244:251], v[98:101]
	v_mfma_f32_16x16x128_f8f6f4 v[90:93], v[26:33], v[244:251], v[90:93]
	s_setprio 0
	s_setprio 1
	v_mfma_f32_16x16x128_f8f6f4 v[62:65], v[2:9], v[220:227], v[62:65]
	v_mfma_f32_16x16x128_f8f6f4 v[58:61], v[10:17], v[220:227], v[58:61]
	v_mfma_f32_16x16x128_f8f6f4 v[54:57], v[2:9], v[228:235], v[54:57]
	v_mfma_f32_16x16x128_f8f6f4 v[50:53], v[10:17], v[228:235], v[50:53]
	v_mfma_f32_16x16x128_f8f6f4 v[46:49], v[2:9], v[236:243], v[46:49]
	v_mfma_f32_16x16x128_f8f6f4 v[42:45], v[10:17], v[236:243], v[42:45]
	v_mfma_f32_16x16x128_f8f6f4 v[38:41], v[2:9], v[244:251], v[38:41]
	v_mfma_f32_16x16x128_f8f6f4 v[34:37], v[10:17], v[244:251], v[34:37]
	s_setprio 0
	s_barrier
.Lp7_blk3:
	ds_read_b128 v[2:5], v210 offset:32768
	ds_read_b128 v[6:9], v211 offset:32768
	ds_read_b128 v[10:13], v210 offset:34816
	ds_read_b128 v[14:17], v211 offset:34816
	ds_read_b128 v[18:21], v210 offset:49152
	ds_read_b128 v[22:25], v211 offset:49152
	ds_read_b128 v[26:29], v210 offset:51200
	ds_read_b128 v[30:33], v211 offset:51200
	s_mov_b32 m0, s41
	v_lshl_add_u64 v[198:199], s[48:49], 0, v[198:199]
	ds_read_b128 v[220:223], v213 offset:32768
	ds_read_b128 v[228:231], v213 offset:34816
	ds_read_b128 v[224:227], v214 offset:32768
	ds_read_b128 v[232:235], v214 offset:34816
	ds_read_b128 v[236:239], v213 offset:36864
	ds_read_b128 v[244:247], v213 offset:38912
	ds_read_b128 v[240:243], v214 offset:36864
	ds_read_b128 v[248:251], v214 offset:38912
	global_load_lds_dwordx4 v[198:199], off
	v_lshl_add_u64 v[196:197], s[48:49], 0, v[196:197]
	s_mov_b32 m0, s53
	v_lshl_add_u64 v[194:195], s[48:49], 0, v[194:195]
	global_load_lds_dwordx4 v[196:197], off
	s_mov_b32 m0, s54
	v_lshl_add_u64 v[192:193], s[48:49], 0, v[192:193]
	global_load_lds_dwordx4 v[194:195], off
	s_mov_b32 m0, s55
	s_nop 0
	global_load_lds_dwordx4 v[192:193], off
	s_waitcnt vmcnt(8)
	s_waitcnt lgkmcnt(0)
	s_barrier
	s_setprio 1
	s_waitcnt lgkmcnt(0)
	v_mfma_f32_16x16x128_f8f6f4 v[158:161], v[2:9], v[220:227], v[158:161]
	v_mfma_f32_16x16x128_f8f6f4 v[154:157], v[10:17], v[220:227], v[154:157]
	v_mfma_f32_16x16x128_f8f6f4 v[150:153], v[2:9], v[228:235], v[150:153]
	v_mfma_f32_16x16x128_f8f6f4 v[146:149], v[10:17], v[228:235], v[146:149]
	v_mfma_f32_16x16x128_f8f6f4 v[142:145], v[2:9], v[236:243], v[142:145]
	v_mfma_f32_16x16x128_f8f6f4 v[138:141], v[10:17], v[236:243], v[138:141]
	v_mfma_f32_16x16x128_f8f6f4 v[134:137], v[2:9], v[244:251], v[134:137]
	v_mfma_f32_16x16x128_f8f6f4 v[130:133], v[10:17], v[244:251], v[130:133]
	s_setprio 0
	s_setprio 1
	v_mfma_f32_16x16x128_f8f6f4 v[102:105], v[18:25], v[220:227], v[102:105]
	v_mfma_f32_16x16x128_f8f6f4 v[94:97], v[26:33], v[220:227], v[94:97]
	v_mfma_f32_16x16x128_f8f6f4 v[86:89], v[18:25], v[228:235], v[86:89]
	v_mfma_f32_16x16x128_f8f6f4 v[82:85], v[26:33], v[228:235], v[82:85]
	v_mfma_f32_16x16x128_f8f6f4 v[78:81], v[18:25], v[236:243], v[78:81]
	v_mfma_f32_16x16x128_f8f6f4 v[74:77], v[26:33], v[236:243], v[74:77]
	v_mfma_f32_16x16x128_f8f6f4 v[70:73], v[18:25], v[244:251], v[70:73]
	v_mfma_f32_16x16x128_f8f6f4 v[66:69], v[26:33], v[244:251], v[66:69]
	s_setprio 0
	s_barrier
	s_add_i32 s48, s70, s51
	v_lshl_add_u64 v[200:201], v[200:201], 0, s[10:11]
	s_mov_b32 m0, s48
	ds_read_b128 v[192:195], v213 offset:49152
	ds_read_b128 v[220:223], v213 offset:51200
	ds_read_b128 v[196:199], v214 offset:49152
	ds_read_b128 v[224:227], v214 offset:51200
	ds_read_b128 v[228:231], v213 offset:53248
	ds_read_b128 v[236:239], v213 offset:55296
	ds_read_b128 v[232:235], v214 offset:53248
	ds_read_b128 v[240:243], v214 offset:55296
	global_load_lds_dwordx4 v[200:201], off
	s_add_i32 m0, s48, 0x2000
	s_add_u32 s46, s46, 0x40080
	v_lshl_add_u64 v[200:201], v[202:203], 0, s[10:11]
	s_addc_u32 s47, s47, 0
	s_add_i32 s48, s72, s51
	global_load_lds_dwordx4 v[200:201], off
	v_lshl_add_u64 v[200:201], s[46:47], 0, v[162:163]
	s_mov_b32 m0, s48
	s_nop 0
	global_load_lds_dwordx4 v[200:201], off
	v_lshl_add_u64 v[200:201], s[46:47], 0, v[164:165]
	s_add_i32 m0, s48, 0x2000
	s_nop 0
	global_load_lds_dwordx4 v[200:201], off
	s_waitcnt vmcnt(6)
	s_waitcnt lgkmcnt(0)
	s_barrier
	s_setprio 1
	s_waitcnt lgkmcnt(0)
	v_mfma_f32_16x16x128_f8f6f4 v[126:129], v[2:9], v[192:199], v[126:129]
	v_mfma_f32_16x16x128_f8f6f4 v[122:125], v[10:17], v[192:199], v[122:125]
	v_mfma_f32_16x16x128_f8f6f4 v[118:121], v[2:9], v[220:227], v[118:121]
	v_mfma_f32_16x16x128_f8f6f4 v[114:117], v[10:17], v[220:227], v[114:117]
	v_mfma_f32_16x16x128_f8f6f4 v[110:113], v[2:9], v[228:235], v[110:113]
	v_mfma_f32_16x16x128_f8f6f4 v[106:109], v[10:17], v[228:235], v[106:109]
	v_mfma_f32_16x16x128_f8f6f4 v[98:101], v[2:9], v[236:243], v[98:101]
	v_mfma_f32_16x16x128_f8f6f4 v[90:93], v[10:17], v[236:243], v[90:93]
	s_setprio 0
	s_setprio 1
	v_mfma_f32_16x16x128_f8f6f4 v[62:65], v[18:25], v[192:199], v[62:65]
	v_mfma_f32_16x16x128_f8f6f4 v[58:61], v[26:33], v[192:199], v[58:61]
	v_mfma_f32_16x16x128_f8f6f4 v[54:57], v[18:25], v[220:227], v[54:57]
	v_mfma_f32_16x16x128_f8f6f4 v[50:53], v[26:33], v[220:227], v[50:53]
	v_mfma_f32_16x16x128_f8f6f4 v[46:49], v[18:25], v[228:235], v[46:49]
	v_mfma_f32_16x16x128_f8f6f4 v[42:45], v[26:33], v[228:235], v[42:45]
	v_mfma_f32_16x16x128_f8f6f4 v[38:41], v[18:25], v[236:243], v[38:41]
	v_mfma_f32_16x16x128_f8f6f4 v[34:37], v[26:33], v[236:243], v[34:37]
	s_setprio 0
	s_barrier
	s_add_i32 s43, s43, 2
	s_add_u32 s44, s44, 0x100
	s_addc_u32 s45, s45, 0
	s_cmp_gt_u32 s43, 13
	s_cbranch_scc1 .LBB0_866
